# code placement: the five steady-loop heads aligned to 64 bytes (pad nops outside the loops, executed once per unit); otherwise stack4
# baseline (speedup 1.0000x reference)
; #define PG8_TRIP_HEAD(T) const int t = (T); const bool last = (t == nt - 2); \
;             const char* a1 = cA + (size_t)(t + 1) * kstep; \
;             const char* a2 = last ? nA : cA + (size_t)(t + 2) * kstep; const char* b2 = last ? nB : cB + (size_t)(t + 2) * kstep; \
;             const char* a3 = a2 + kstep; const char* b3 = b2 + kstep; \
;             if (last && has_next) S.a_ready(nxt);
; template <class Epi, class Sched, bool ALIGN_EPI = false, bool SP2 = false>
; __device__ __forceinline__ void gemm_phase(PG8_LAS unsigned char* lds, const Gemm g, const Sched& S, const Epi& E) {
;     ...
;             { PG8_TRIP_HEAD(0) PG8_TRIP_SP2(asm volatile("s_waitcnt vmcnt(%0)" :: "n"(8 + Epi::NST) : "memory"), PG8_MMAZ) }
.LBB0_129:
	s_ashr_i32 s23, s22, 31
	s_lshl_b64 s[4:5], s[22:23], 20
	s_add_u32 s26, s34, s4
	s_addc_u32 s27, s35, s5
	s_add_i32 s45, 0, 0x10000
	s_add_i32 s47, 0, 0x14000
	v_add_u32_e32 v140, s45, v160
	v_add_u32_e32 v141, s47, v160
	ds_read_b128 v[4:7], v140
	ds_read_b128 v[8:11], v140 offset:1024
	ds_read_b128 v[12:15], v140 offset:2048
	ds_read_b128 v[16:19], v140 offset:3072
	ds_read_b128 v[20:23], v141
	ds_read_b128 v[24:27], v141 offset:1024
	ds_read_b128 v[28:31], v141 offset:2048
	ds_read_b128 v[32:35], v141 offset:3072
	s_and_b64 s[4:5], s[10:11], exec
	s_cselect_b32 s4, s27, s29
	s_cselect_b32 s5, s26, s28
	v_lshl_add_u64 v[184:185], s[30:31], 0, v[134:135]
	s_mov_b64 s[10:11], 0x84080
	s_add_i32 s23, s37, 0xc000
	v_lshl_add_u64 v[68:69], v[184:185], 0, s[10:11]
	s_mov_b32 m0, s23
	s_mov_b64 s[10:11], 0xc6080
	s_add_i32 s33, s37, 0xe000
	ds_read_b128 v[36:39], v163
	ds_read_b128 v[40:43], v163 offset:1024
	ds_read_b128 v[44:47], v163 offset:2048
	ds_read_b128 v[48:51], v163 offset:3072
	ds_read_b128 v[52:55], v163 offset:4096
	ds_read_b128 v[56:59], v163 offset:5120
	ds_read_b128 v[60:63], v163 offset:6144
	ds_read_b128 v[64:67], v163 offset:7168
	global_load_lds_dwordx4 v[68:69], off
	v_lshl_add_u64 v[68:69], v[184:185], 0, s[10:11]
	s_mov_b32 m0, s33
	s_nop 0
	global_load_lds_dwordx4 v[68:69], off
	s_waitcnt vmcnt(16)
	s_waitcnt lgkmcnt(0)
	s_barrier
	v_mfma_f32_16x16x32_bf16 v[88:91], v[12:15], v[52:55], 0
	v_mfma_f32_16x16x32_bf16 v[92:95], v[16:19], v[56:59], v[88:91]
	v_mfma_f32_16x16x32_bf16 v[88:91], v[4:7], v[60:63], 0
	v_mfma_f32_16x16x32_bf16 v[68:71], v[4:7], v[36:39], 0
	v_mfma_f32_16x16x32_bf16 v[72:75], v[12:15], v[36:39], 0
	v_mfma_f32_16x16x32_bf16 v[76:79], v[4:7], v[44:47], 0
	v_mfma_f32_16x16x32_bf16 v[80:83], v[12:15], v[44:47], 0
	v_mfma_f32_16x16x32_bf16 v[84:87], v[4:7], v[52:55], 0
	v_mfma_f32_16x16x32_bf16 v[96:99], v[8:11], v[64:67], v[88:91]
	v_mfma_f32_16x16x32_bf16 v[88:91], v[12:15], v[60:63], 0
	v_mfma_f32_16x16x32_bf16 v[68:71], v[8:11], v[40:43], v[68:71]
	v_mfma_f32_16x16x32_bf16 v[72:75], v[16:19], v[40:43], v[72:75]
	v_mfma_f32_16x16x32_bf16 v[76:79], v[8:11], v[48:51], v[76:79]
	v_mfma_f32_16x16x32_bf16 v[80:83], v[16:19], v[48:51], v[80:83]
	v_mfma_f32_16x16x32_bf16 v[84:87], v[8:11], v[56:59], v[84:87]
	v_mfma_f32_16x16x32_bf16 v[108:111], v[16:19], v[64:67], v[88:91]
	v_mfma_f32_16x16x32_bf16 v[88:91], v[20:23], v[36:39], 0
	v_mfma_f32_16x16x32_bf16 v[36:39], v[28:31], v[36:39], 0
	v_mfma_f32_16x16x32_bf16 v[112:115], v[24:27], v[40:43], v[88:91]
	v_mfma_f32_16x16x32_bf16 v[36:39], v[32:35], v[40:43], v[36:39]
	v_mfma_f32_16x16x32_bf16 v[40:43], v[20:23], v[44:47], 0
	v_mfma_f32_16x16x32_bf16 v[44:47], v[28:31], v[44:47], 0
	v_mfma_f32_16x16x32_bf16 v[40:43], v[24:27], v[48:51], v[40:43]
	v_mfma_f32_16x16x32_bf16 v[44:47], v[32:35], v[48:51], v[44:47]
	v_mfma_f32_16x16x32_bf16 v[48:51], v[20:23], v[52:55], 0
	v_mfma_f32_16x16x32_bf16 v[52:55], v[28:31], v[52:55], 0
	v_mfma_f32_16x16x32_bf16 v[48:51], v[24:27], v[56:59], v[48:51]
	v_mfma_f32_16x16x32_bf16 v[52:55], v[32:35], v[56:59], v[52:55]
	v_mfma_f32_16x16x32_bf16 v[56:59], v[20:23], v[60:63], 0
	v_mfma_f32_16x16x32_bf16 v[60:63], v[28:31], v[60:63], 0
	v_mfma_f32_16x16x32_bf16 v[56:59], v[24:27], v[64:67], v[56:59]
	v_mfma_f32_16x16x32_bf16 v[60:63], v[32:35], v[64:67], v[60:63]
	s_barrier
	v_lshl_add_u64 v[186:187], s[28:29], 0, v[132:133]
	s_mov_b64 s[10:11], 0x100
	s_add_i32 s45, s45, s36
	v_lshl_add_u64 v[142:143], v[186:187], 0, s[10:11]
	s_mov_b32 m0, s45
	s_mov_b64 s[48:49], 0x40100
	s_add_i32 s46, s45, 0x2000
	ds_read_b128 v[64:67], v163 offset:16384
	ds_read_b128 v[88:91], v163 offset:17408
	ds_read_b128 v[100:103], v163 offset:18432
	ds_read_b128 v[104:107], v163 offset:19456
	ds_read_b128 v[116:119], v163 offset:20480
	ds_read_b128 v[120:123], v163 offset:21504
	ds_read_b128 v[124:127], v163 offset:22528
	ds_read_b128 v[128:131], v163 offset:23552
	global_load_lds_dwordx4 v[142:143], off
	v_lshl_add_u64 v[142:143], v[186:187], 0, s[48:49]
	s_mov_b32 m0, s46
	s_mov_b64 s[48:49], 0x80100
	s_add_i32 s47, s47, s36
	global_load_lds_dwordx4 v[142:143], off
	v_lshl_add_u64 v[142:143], v[186:187], 0, s[48:49]
	s_mov_b32 m0, s47
	s_mov_b64 s[48:49], 0xc0100
	global_load_lds_dwordx4 v[142:143], off
	v_lshl_add_u64 v[142:143], v[186:187], 0, s[48:49]
	s_add_i32 s48, s47, 0x2000
	s_mov_b32 m0, s48
	s_nop 0
	global_load_lds_dwordx4 v[142:143], off
	v_lshl_add_u64 v[142:143], v[184:185], 0, s[10:11]
	s_mov_b32 m0, s37
	s_mov_b64 s[10:11], 0x42100
	global_load_lds_dwordx4 v[142:143], off
	v_lshl_add_u64 v[142:143], v[184:185], 0, s[10:11]
	s_mov_b32 m0, s38
	s_nop 0
	global_load_lds_dwordx4 v[142:143], off
	s_waitcnt vmcnt(16)
	s_waitcnt lgkmcnt(0)
	s_barrier
	v_mfma_f32_16x16x32_bf16 v[142:145], v[4:7], v[64:67], 0
	v_mfma_f32_16x16x32_bf16 v[152:155], v[4:7], v[100:103], 0
	v_mfma_f32_16x16x32_bf16 v[164:167], v[4:7], v[116:119], 0
	v_mfma_f32_16x16x32_bf16 v[4:7], v[4:7], v[124:127], 0
	v_mfma_f32_16x16x32_bf16 v[144:147], v[8:11], v[88:91], v[142:145]
	v_mfma_f32_16x16x32_bf16 v[152:155], v[8:11], v[104:107], v[152:155]
	v_mfma_f32_16x16x32_bf16 v[164:167], v[8:11], v[120:123], v[164:167]
	v_mfma_f32_16x16x32_bf16 v[4:7], v[8:11], v[128:131], v[4:7]
	v_mfma_f32_16x16x32_bf16 v[8:11], v[12:15], v[124:127], 0
	v_mfma_f32_16x16x32_bf16 v[148:151], v[12:15], v[64:67], 0
	v_mfma_f32_16x16x32_bf16 v[156:159], v[12:15], v[100:103], 0
	v_mfma_f32_16x16x32_bf16 v[168:171], v[12:15], v[116:119], 0
	v_mfma_f32_16x16x32_bf16 v[12:15], v[16:19], v[128:131], v[8:11]
	v_mfma_f32_16x16x32_bf16 v[148:151], v[16:19], v[88:91], v[148:151]
	v_mfma_f32_16x16x32_bf16 v[156:159], v[16:19], v[104:107], v[156:159]
	v_mfma_f32_16x16x32_bf16 v[168:171], v[16:19], v[120:123], v[168:171]
	v_mfma_f32_16x16x32_bf16 v[8:11], v[20:23], v[64:67], 0
	v_mfma_f32_16x16x32_bf16 v[16:19], v[24:27], v[88:91], v[8:11]
	v_mfma_f32_16x16x32_bf16 v[8:11], v[28:31], v[64:67], 0
	v_mfma_f32_16x16x32_bf16 v[172:175], v[32:35], v[88:91], v[8:11]
	v_mfma_f32_16x16x32_bf16 v[8:11], v[20:23], v[100:103], 0
	v_mfma_f32_16x16x32_bf16 v[176:179], v[24:27], v[104:107], v[8:11]
	v_mfma_f32_16x16x32_bf16 v[8:11], v[28:31], v[100:103], 0
	v_mfma_f32_16x16x32_bf16 v[194:197], v[32:35], v[104:107], v[8:11]
	v_mfma_f32_16x16x32_bf16 v[8:11], v[20:23], v[116:119], 0
	v_mfma_f32_16x16x32_bf16 v[198:201], v[24:27], v[120:123], v[8:11]
	v_mfma_f32_16x16x32_bf16 v[8:11], v[28:31], v[116:119], 0
	v_mfma_f32_16x16x32_bf16 v[202:205], v[32:35], v[120:123], v[8:11]
	v_mfma_f32_16x16x32_bf16 v[8:11], v[20:23], v[124:127], 0
	v_mfma_f32_16x16x32_bf16 v[206:209], v[24:27], v[128:131], v[8:11]
	v_mfma_f32_16x16x32_bf16 v[8:11], v[28:31], v[124:127], 0
	v_mfma_f32_16x16x32_bf16 v[220:223], v[32:35], v[128:131], v[8:11]
	s_barrier
	s_add_i32 s49, 0, 0x18000
	s_add_i32 s51, 0, 0x1c000
	v_add_u32_e32 v142, s49, v160
	v_add_u32_e32 v143, s51, v160
	s_nop 0
	ds_read_b128 v[8:11], v142
	ds_read_b128 v[28:31], v142 offset:1024
	ds_read_b128 v[32:35], v142 offset:2048
	ds_read_b128 v[64:67], v142 offset:3072
	ds_read_b128 v[224:227], v143
	ds_read_b128 v[228:231], v143 offset:1024
	ds_read_b128 v[232:235], v143 offset:2048
	ds_read_b128 v[236:239], v143 offset:3072
	s_mov_b64 s[10:11], 0x84100
	s_mov_b32 m0, s39
	v_lshl_add_u64 v[88:89], v[184:185], 0, s[10:11]
	s_mov_b64 s[10:11], 0xc6100
	ds_read_b128 v[20:23], v163 offset:32768
	ds_read_b128 v[24:27], v163 offset:33792
	ds_read_b128 v[240:243], v163 offset:34816
	ds_read_b128 v[244:247], v163 offset:35840
	ds_read_b128 v[248:251], v163 offset:36864
	ds_read_b128 v[216:219], v163 offset:37888
	ds_read_b128 v[190:193], v163 offset:38912
	ds_read_b128 v[180:183], v163 offset:39936
	global_load_lds_dwordx4 v[88:89], off
	v_lshl_add_u64 v[88:89], v[184:185], 0, s[10:11]
	s_mov_b32 m0, s40
	s_nop 0
	global_load_lds_dwordx4 v[88:89], off
	s_waitcnt vmcnt(8)
	s_waitcnt lgkmcnt(0)
	s_barrier
	v_mfma_f32_16x16x32_bf16 v[68:71], v[8:11], v[20:23], v[68:71]
	v_mfma_f32_16x16x32_bf16 v[120:123], v[28:31], v[24:27], v[68:71]
	v_mfma_f32_16x16x32_bf16 v[68:71], v[32:35], v[20:23], v[72:75]
	v_mfma_f32_16x16x32_bf16 v[116:119], v[64:67], v[24:27], v[68:71]
	v_mfma_f32_16x16x32_bf16 v[68:71], v[8:11], v[240:243], v[76:79]
	v_mfma_f32_16x16x32_bf16 v[104:107], v[28:31], v[244:247], v[68:71]
	v_mfma_f32_16x16x32_bf16 v[68:71], v[32:35], v[240:243], v[80:83]
	v_mfma_f32_16x16x32_bf16 v[100:103], v[64:67], v[244:247], v[68:71]
	v_mfma_f32_16x16x32_bf16 v[68:71], v[8:11], v[248:251], v[84:87]
	v_mfma_f32_16x16x32_bf16 v[88:91], v[28:31], v[216:219], v[68:71]
	v_mfma_f32_16x16x32_bf16 v[68:71], v[32:35], v[248:251], v[92:95]
	v_mfma_f32_16x16x32_bf16 v[84:87], v[64:67], v[216:219], v[68:71]
	v_mfma_f32_16x16x32_bf16 v[68:71], v[8:11], v[190:193], v[96:99]
	v_mfma_f32_16x16x32_bf16 v[72:75], v[28:31], v[180:183], v[68:71]
	v_mfma_f32_16x16x32_bf16 v[68:71], v[32:35], v[190:193], v[108:111]
	v_mfma_f32_16x16x32_bf16 v[68:71], v[64:67], v[180:183], v[68:71]
	v_mfma_f32_16x16x32_bf16 v[76:79], v[224:227], v[20:23], v[112:115]
	v_mfma_f32_16x16x32_bf16 v[20:23], v[232:235], v[20:23], v[36:39]
	v_mfma_f32_16x16x32_bf16 v[124:127], v[236:239], v[24:27], v[20:23]
	v_mfma_f32_16x16x32_bf16 v[20:23], v[224:227], v[240:243], v[40:43]
	v_mfma_f32_16x16x32_bf16 v[112:115], v[228:231], v[244:247], v[20:23]
	v_mfma_f32_16x16x32_bf16 v[20:23], v[232:235], v[240:243], v[44:47]
	v_mfma_f32_16x16x32_bf16 v[108:111], v[236:239], v[244:247], v[20:23]
	v_mfma_f32_16x16x32_bf16 v[20:23], v[224:227], v[248:251], v[48:51]
	v_mfma_f32_16x16x32_bf16 v[96:99], v[228:231], v[216:219], v[20:23]
	v_mfma_f32_16x16x32_bf16 v[20:23], v[232:235], v[248:251], v[52:55]
	v_mfma_f32_16x16x32_bf16 v[92:95], v[236:239], v[216:219], v[20:23]
	v_mfma_f32_16x16x32_bf16 v[20:23], v[224:227], v[190:193], v[56:59]
	v_mfma_f32_16x16x32_bf16 v[80:83], v[228:231], v[180:183], v[20:23]
	v_mfma_f32_16x16x32_bf16 v[20:23], v[232:235], v[190:193], v[60:63]
	v_mfma_f32_16x16x32_bf16 v[128:131], v[228:231], v[24:27], v[76:79]
	v_mfma_f32_16x16x32_bf16 v[76:79], v[236:239], v[180:183], v[20:23]
	s_barrier
; #define PG8_MMA(ai, bj, At, Bt) do { __builtin_amdgcn_s_setprio(1); _Pragma("unroll") for (int m = 0; m < 4; ++m) _Pragma("unroll") for (int n = 0; n < 2; ++n) _Pragma("unroll") for (int k = 0; k < 2; ++k) \
;         acc[ai][bj][m][n] = __builtin_amdgcn_mfma_f32_16x16x32_bf16(Bt[n][k], At[m][k], acc[ai][bj][m][n], 0, 0, 0); __builtin_amdgcn_s_setprio(0); } while (0)
; #define PG8_WAIT_V(n) asm volatile("s_waitcnt vmcnt(" #n ")" ::: "memory")
; #define PG8_TRIP_HEAD(T) const int t = (T); const bool last = (t == nt - 2); \
;             const char* a1 = cA + (size_t)(t + 1) * kstep; \
;             const char* a2 = last ? nA : cA + (size_t)(t + 2) * kstep; const char* b2 = last ? nB : cB + (size_t)(t + 2) * kstep; \
;             const char* a3 = a2 + kstep; const char* b3 = b2 + kstep; \
;             if (last && has_next) S.a_ready(nxt);
; template <class Epi, class Sched, bool ALIGN_EPI = false, bool SP2 = false>
; __device__ __forceinline__ void gemm_phase(PG8_LAS unsigned char* lds, const Gemm g, const Sched& S, const Epi& E) {
;     ...
;         if constexpr (SP2) {
;             { PG8_TRIP_HEAD(0) PG8_TRIP_SP2(asm volatile("s_waitcnt vmcnt(%0)" :: "n"(8 + Epi::NST) : "memory"), PG8_MMAZ) }
;             for (int tt = 2; tt < nt; tt += 2) { PG8_TRIP_HEAD(tt) PG8_TRIP_SP2(PG8_WAIT_V(8), PG8_MMA) }
	s_mov_b64 s[10:11], 0x180
	s_add_i32 s49, s49, s36
	s_nop 1
	v_lshl_add_u64 v[20:21], v[186:187], 0, s[10:11]
	s_mov_b32 m0, s49
	s_mov_b64 s[52:53], 0x40180
	s_add_i32 s50, s49, 0x2000
	ds_read_b128 v[44:47], v163 offset:49152
	ds_read_b128 v[48:51], v163 offset:50176
	ds_read_b128 v[180:183], v163 offset:51200
	ds_read_b128 v[190:193], v163 offset:52224
	ds_read_b128 v[216:219], v163 offset:53248
	ds_read_b128 v[240:243], v163 offset:54272
	ds_read_b128 v[244:247], v163 offset:55296
	ds_read_b128 v[248:251], v163 offset:56320
	global_load_lds_dwordx4 v[20:21], off
	v_lshl_add_u64 v[20:21], v[186:187], 0, s[52:53]
	s_mov_b32 m0, s50
	s_mov_b64 s[52:53], 0x80180
	s_add_i32 s51, s51, s36
	global_load_lds_dwordx4 v[20:21], off
	v_lshl_add_u64 v[20:21], v[186:187], 0, s[52:53]
	s_mov_b32 m0, s51
	s_mov_b64 s[52:53], 0xc0180
	global_load_lds_dwordx4 v[20:21], off
	v_lshl_add_u64 v[20:21], v[186:187], 0, s[52:53]
	s_add_i32 s52, s51, 0x2000
	s_mov_b32 m0, s52
	s_nop 0
	global_load_lds_dwordx4 v[20:21], off
	v_lshl_add_u64 v[20:21], v[184:185], 0, s[10:11]
	s_mov_b32 m0, s0
	s_mov_b64 s[10:11], 0x42180
	global_load_lds_dwordx4 v[20:21], off
	v_lshl_add_u64 v[20:21], v[184:185], 0, s[10:11]
	s_mov_b32 m0, s41
	s_nop 0
	global_load_lds_dwordx4 v[20:21], off
	s_waitcnt vmcnt(8)
	s_waitcnt lgkmcnt(0)
	s_barrier
	v_mfma_f32_16x16x32_bf16 v[20:23], v[8:11], v[44:47], v[144:147]
	v_mfma_f32_16x16x32_bf16 v[56:59], v[28:31], v[48:51], v[20:23]
	v_mfma_f32_16x16x32_bf16 v[20:23], v[32:35], v[44:47], v[148:151]
	v_mfma_f32_16x16x32_bf16 v[52:55], v[64:67], v[48:51], v[20:23]
	v_mfma_f32_16x16x32_bf16 v[20:23], v[8:11], v[180:183], v[152:155]
	v_mfma_f32_16x16x32_bf16 v[40:43], v[28:31], v[190:193], v[20:23]
	v_mfma_f32_16x16x32_bf16 v[20:23], v[32:35], v[180:183], v[156:159]
	v_mfma_f32_16x16x32_bf16 v[36:39], v[64:67], v[190:193], v[20:23]
	v_mfma_f32_16x16x32_bf16 v[20:23], v[8:11], v[216:219], v[164:167]
	v_mfma_f32_16x16x32_bf16 v[4:7], v[8:11], v[244:247], v[4:7]
	v_mfma_f32_16x16x32_bf16 v[24:27], v[28:31], v[240:243], v[20:23]
	v_mfma_f32_16x16x32_bf16 v[20:23], v[32:35], v[216:219], v[168:171]
	v_mfma_f32_16x16x32_bf16 v[8:11], v[28:31], v[248:251], v[4:7]
	v_mfma_f32_16x16x32_bf16 v[4:7], v[32:35], v[244:247], v[12:15]
	v_mfma_f32_16x16x32_bf16 v[20:23], v[64:67], v[240:243], v[20:23]
	v_mfma_f32_16x16x32_bf16 v[4:7], v[64:67], v[248:251], v[4:7]
	v_mfma_f32_16x16x32_bf16 v[12:15], v[224:227], v[44:47], v[16:19]
	v_mfma_f32_16x16x32_bf16 v[64:67], v[228:231], v[48:51], v[12:15]
	v_mfma_f32_16x16x32_bf16 v[12:15], v[232:235], v[44:47], v[172:175]
	v_mfma_f32_16x16x32_bf16 v[60:63], v[236:239], v[48:51], v[12:15]
	v_mfma_f32_16x16x32_bf16 v[12:15], v[224:227], v[180:183], v[176:179]
	v_mfma_f32_16x16x32_bf16 v[48:51], v[228:231], v[190:193], v[12:15]
	v_mfma_f32_16x16x32_bf16 v[12:15], v[232:235], v[180:183], v[194:197]
	v_mfma_f32_16x16x32_bf16 v[44:47], v[236:239], v[190:193], v[12:15]
	v_mfma_f32_16x16x32_bf16 v[12:15], v[224:227], v[216:219], v[198:201]
	v_mfma_f32_16x16x32_bf16 v[32:35], v[228:231], v[240:243], v[12:15]
	v_mfma_f32_16x16x32_bf16 v[12:15], v[232:235], v[216:219], v[202:205]
	v_mfma_f32_16x16x32_bf16 v[28:31], v[236:239], v[240:243], v[12:15]
	v_mfma_f32_16x16x32_bf16 v[12:15], v[224:227], v[244:247], v[206:209]
	v_mfma_f32_16x16x32_bf16 v[16:19], v[228:231], v[248:251], v[12:15]
	v_mfma_f32_16x16x32_bf16 v[12:15], v[232:235], v[244:247], v[220:223]
	v_mfma_f32_16x16x32_bf16 v[12:15], v[236:239], v[248:251], v[12:15]
	s_barrier
	s_add_u32 s10, s30, 0x84180
	s_addc_u32 s11, s31, 0
	s_add_u32 s28, s28, 0x200
	s_addc_u32 s29, s29, 0
	s_mov_b32 s30, 0
	s_mov_b64 s[60:61], 0x80000
	s_mov_b64 s[62:63], 0x80080
	s_mov_b64 s[64:65], 0xc0000
	s_mov_b64 s[66:67], 0xc0080
	s_mov_b64 s[68:69], 0xc6000
	.p2align	6

.LBB0_232:
	s_add_i32 s5, 0, 0x10000
	s_add_i32 s42, 0, 0x14000
	v_add_u32_e32 v116, s5, v176
	v_add_u32_e32 v117, s42, v176
	ds_read_b128 v[4:7], v116
	ds_read_b128 v[8:11], v116 offset:1024
	ds_read_b128 v[12:15], v116 offset:2048
	ds_read_b128 v[16:19], v116 offset:3072
	ds_read_b128 v[20:23], v117
	ds_read_b128 v[24:27], v117 offset:1024
	ds_read_b128 v[28:31], v117 offset:2048
	ds_read_b128 v[32:35], v117 offset:3072
	v_lshl_add_u64 v[188:189], s[26:27], 0, v[160:161]
	s_mov_b64 s[62:63], 0x160080
	s_add_i32 s0, s31, 0xc000
	v_lshl_add_u64 v[68:69], v[188:189], 0, s[62:63]
	s_mov_b32 m0, s0
	s_mov_b64 s[64:65], 0x210080
	s_add_i32 s4, s31, 0xe000
	ds_read_b128 v[36:39], v178
	ds_read_b128 v[40:43], v178 offset:1024
	ds_read_b128 v[44:47], v178 offset:2048
	ds_read_b128 v[48:51], v178 offset:3072
	ds_read_b128 v[52:55], v178 offset:4096
	ds_read_b128 v[56:59], v178 offset:5120
	ds_read_b128 v[60:63], v178 offset:6144
	ds_read_b128 v[64:67], v178 offset:7168
	global_load_lds_dwordx4 v[68:69], off
	v_lshl_add_u64 v[68:69], v[188:189], 0, s[64:65]
	s_mov_b32 m0, s4
	s_nop 0
	global_load_lds_dwordx4 v[68:69], off
	s_waitcnt vmcnt(16)
	s_waitcnt lgkmcnt(0)
	s_barrier
	v_mfma_f32_16x16x32_bf16 v[92:95], v[4:7], v[60:63], 0
	v_mfma_f32_16x16x32_bf16 v[68:71], v[4:7], v[36:39], 0
	v_mfma_f32_16x16x32_bf16 v[72:75], v[12:15], v[36:39], 0
	v_mfma_f32_16x16x32_bf16 v[76:79], v[4:7], v[44:47], 0
	v_mfma_f32_16x16x32_bf16 v[80:83], v[12:15], v[44:47], 0
	v_mfma_f32_16x16x32_bf16 v[84:87], v[4:7], v[52:55], 0
	v_mfma_f32_16x16x32_bf16 v[88:91], v[12:15], v[52:55], 0
	v_mfma_f32_16x16x32_bf16 v[100:103], v[8:11], v[64:67], v[92:95]
	v_mfma_f32_16x16x32_bf16 v[92:95], v[12:15], v[60:63], 0
	v_mfma_f32_16x16x32_bf16 v[68:71], v[8:11], v[40:43], v[68:71]
	v_mfma_f32_16x16x32_bf16 v[72:75], v[16:19], v[40:43], v[72:75]
	v_mfma_f32_16x16x32_bf16 v[76:79], v[8:11], v[48:51], v[76:79]
	v_mfma_f32_16x16x32_bf16 v[80:83], v[16:19], v[48:51], v[80:83]
	v_mfma_f32_16x16x32_bf16 v[84:87], v[8:11], v[56:59], v[84:87]
	v_mfma_f32_16x16x32_bf16 v[88:91], v[16:19], v[56:59], v[88:91]
	v_mfma_f32_16x16x32_bf16 v[104:107], v[16:19], v[64:67], v[92:95]
	v_mfma_f32_16x16x32_bf16 v[92:95], v[20:23], v[36:39], 0
	v_mfma_f32_16x16x32_bf16 v[36:39], v[28:31], v[36:39], 0
	v_mfma_f32_16x16x32_bf16 v[120:123], v[24:27], v[40:43], v[92:95]
	v_mfma_f32_16x16x32_bf16 v[36:39], v[32:35], v[40:43], v[36:39]
	v_mfma_f32_16x16x32_bf16 v[40:43], v[20:23], v[44:47], 0
	v_mfma_f32_16x16x32_bf16 v[44:47], v[28:31], v[44:47], 0
	v_mfma_f32_16x16x32_bf16 v[40:43], v[24:27], v[48:51], v[40:43]
	v_mfma_f32_16x16x32_bf16 v[44:47], v[32:35], v[48:51], v[44:47]
	v_mfma_f32_16x16x32_bf16 v[48:51], v[20:23], v[52:55], 0
	v_mfma_f32_16x16x32_bf16 v[52:55], v[28:31], v[52:55], 0
	v_mfma_f32_16x16x32_bf16 v[48:51], v[24:27], v[56:59], v[48:51]
	v_mfma_f32_16x16x32_bf16 v[52:55], v[32:35], v[56:59], v[52:55]
	v_mfma_f32_16x16x32_bf16 v[56:59], v[20:23], v[60:63], 0
	v_mfma_f32_16x16x32_bf16 v[60:63], v[28:31], v[60:63], 0
	v_mfma_f32_16x16x32_bf16 v[56:59], v[24:27], v[64:67], v[56:59]
	v_mfma_f32_16x16x32_bf16 v[60:63], v[32:35], v[64:67], v[60:63]
	s_barrier
	v_lshl_add_u64 v[214:215], s[24:25], 0, v[162:163]
	s_mov_b64 s[44:45], 0x100
	s_add_i32 s5, s5, s30
	v_lshl_add_u64 v[118:119], v[214:215], 0, s[44:45]
	s_mov_b32 m0, s5
	s_mov_b64 s[46:47], 0xb0100
	s_add_i32 s33, s5, 0x2000
	ds_read_b128 v[64:67], v178 offset:16384
	ds_read_b128 v[92:95], v178 offset:17408
	ds_read_b128 v[96:99], v178 offset:18432
	ds_read_b128 v[108:111], v178 offset:19456
	ds_read_b128 v[112:115], v178 offset:20480
	ds_read_b128 v[124:127], v178 offset:21504
	ds_read_b128 v[128:131], v178 offset:22528
	ds_read_b128 v[132:135], v178 offset:23552
	global_load_lds_dwordx4 v[118:119], off
	v_lshl_add_u64 v[118:119], v[214:215], 0, s[46:47]
	s_mov_b32 m0, s33
	s_mov_b64 s[50:51], 0x160100
	s_add_i32 s42, s42, s30
	global_load_lds_dwordx4 v[118:119], off
	v_lshl_add_u64 v[118:119], v[214:215], 0, s[50:51]
	s_mov_b32 m0, s42
	s_mov_b64 s[52:53], 0x210100
	s_add_i32 s43, s42, 0x2000
	global_load_lds_dwordx4 v[118:119], off
	v_lshl_add_u64 v[118:119], v[214:215], 0, s[52:53]
	s_mov_b32 m0, s43
	s_nop 0
	global_load_lds_dwordx4 v[118:119], off
	v_lshl_add_u64 v[118:119], v[188:189], 0, s[44:45]
	s_mov_b32 m0, s31
	s_nop 0
	global_load_lds_dwordx4 v[118:119], off
	v_lshl_add_u64 v[118:119], v[188:189], 0, s[46:47]
	s_mov_b32 m0, s34
	s_nop 0
	global_load_lds_dwordx4 v[118:119], off
	s_waitcnt vmcnt(16)
	s_waitcnt lgkmcnt(0)
	s_barrier
	v_mfma_f32_16x16x32_bf16 v[136:139], v[4:7], v[64:67], 0
	v_mfma_f32_16x16x32_bf16 v[144:147], v[8:11], v[92:95], v[136:139]
	v_mfma_f32_16x16x32_bf16 v[136:139], v[12:15], v[64:67], 0
	v_mfma_f32_16x16x32_bf16 v[148:151], v[16:19], v[92:95], v[136:139]
	v_mfma_f32_16x16x32_bf16 v[136:139], v[4:7], v[96:99], 0
	v_mfma_f32_16x16x32_bf16 v[152:155], v[8:11], v[108:111], v[136:139]
	v_mfma_f32_16x16x32_bf16 v[136:139], v[12:15], v[96:99], 0
	v_mfma_f32_16x16x32_bf16 v[156:159], v[16:19], v[108:111], v[136:139]
	v_mfma_f32_16x16x32_bf16 v[136:139], v[4:7], v[112:115], 0
	v_mfma_f32_16x16x32_bf16 v[4:7], v[4:7], v[128:131], 0
	v_mfma_f32_16x16x32_bf16 v[166:169], v[8:11], v[124:127], v[136:139]
	v_mfma_f32_16x16x32_bf16 v[4:7], v[8:11], v[132:135], v[4:7]
	v_mfma_f32_16x16x32_bf16 v[8:11], v[12:15], v[128:131], 0
	v_mfma_f32_16x16x32_bf16 v[136:139], v[12:15], v[112:115], 0
	v_mfma_f32_16x16x32_bf16 v[8:11], v[16:19], v[132:135], v[8:11]
	v_mfma_f32_16x16x32_bf16 v[170:173], v[16:19], v[124:127], v[136:139]
	v_mfma_f32_16x16x32_bf16 v[12:15], v[20:23], v[64:67], 0
	v_mfma_f32_16x16x32_bf16 v[180:183], v[24:27], v[92:95], v[12:15]
	v_mfma_f32_16x16x32_bf16 v[12:15], v[28:31], v[64:67], 0
	v_mfma_f32_16x16x32_bf16 v[190:193], v[32:35], v[92:95], v[12:15]
	v_mfma_f32_16x16x32_bf16 v[12:15], v[20:23], v[96:99], 0
	v_mfma_f32_16x16x32_bf16 v[194:197], v[24:27], v[108:111], v[12:15]
	v_mfma_f32_16x16x32_bf16 v[12:15], v[28:31], v[96:99], 0
	v_mfma_f32_16x16x32_bf16 v[198:201], v[32:35], v[108:111], v[12:15]
	v_mfma_f32_16x16x32_bf16 v[12:15], v[20:23], v[112:115], 0
	v_mfma_f32_16x16x32_bf16 v[202:205], v[24:27], v[124:127], v[12:15]
	v_mfma_f32_16x16x32_bf16 v[12:15], v[28:31], v[112:115], 0
	v_mfma_f32_16x16x32_bf16 v[206:209], v[32:35], v[124:127], v[12:15]
	v_mfma_f32_16x16x32_bf16 v[12:15], v[20:23], v[128:131], 0
	v_mfma_f32_16x16x32_bf16 v[216:219], v[24:27], v[132:135], v[12:15]
	v_mfma_f32_16x16x32_bf16 v[12:15], v[28:31], v[128:131], 0
	v_mfma_f32_16x16x32_bf16 v[132:135], v[32:35], v[132:135], v[12:15]
	s_barrier
; #define PG8_MMA(ai, bj, At, Bt) do { __builtin_amdgcn_s_setprio(1); _Pragma("unroll") for (int m = 0; m < 4; ++m) _Pragma("unroll") for (int n = 0; n < 2; ++n) _Pragma("unroll") for (int k = 0; k < 2; ++k) \
;         acc[ai][bj][m][n] = __builtin_amdgcn_mfma_f32_16x16x32_bf16(Bt[n][k], At[m][k], acc[ai][bj][m][n], 0, 0, 0); __builtin_amdgcn_s_setprio(0); } while (0)
; #define PG8_WAIT_V(n) asm volatile("s_waitcnt vmcnt(" #n ")" ::: "memory")
; #define PG8_TRIP_HEAD(T) const int t = (T); const bool last = (t == nt - 2); \
;             const char* a1 = cA + (size_t)(t + 1) * kstep; \
;             const char* a2 = last ? nA : cA + (size_t)(t + 2) * kstep; const char* b2 = last ? nB : cB + (size_t)(t + 2) * kstep; \
;             const char* a3 = a2 + kstep; const char* b3 = b2 + kstep; \
;             if (last && has_next) S.a_ready(nxt);
; template <class Epi, class Sched, bool ALIGN_EPI = false, bool SP2 = false>
; __device__ __forceinline__ void gemm_phase(PG8_LAS unsigned char* lds, const Gemm g, const Sched& S, const Epi& E) {
;     ...
;         if constexpr (SP2) {
;             { PG8_TRIP_HEAD(0) PG8_TRIP_SP2(asm volatile("s_waitcnt vmcnt(%0)" :: "n"(8 + Epi::NST) : "memory"), PG8_MMAZ) }
;             for (int tt = 2; tt < nt; tt += 2) { PG8_TRIP_HEAD(tt) PG8_TRIP_SP2(PG8_WAIT_V(8), PG8_MMA) }
	s_add_i32 s44, 0, 0x18000
	s_add_i32 s48, 0, 0x1c000
	v_add_u32_e32 v118, s44, v176
	v_add_u32_e32 v119, s48, v176
	s_nop 0
	ds_read_b128 v[12:15], v118
	ds_read_b128 v[16:19], v118 offset:1024
	ds_read_b128 v[20:23], v118 offset:2048
	ds_read_b128 v[24:27], v118 offset:3072
	ds_read_b128 v[220:223], v119
	ds_read_b128 v[224:227], v119 offset:1024
	ds_read_b128 v[228:231], v119 offset:2048
	ds_read_b128 v[232:235], v119 offset:3072
	s_mov_b32 m0, s35
	v_lshl_add_u64 v[92:93], v[188:189], 0, s[50:51]
	ds_read_b128 v[28:31], v178 offset:32768
	ds_read_b128 v[32:35], v178 offset:33792
	ds_read_b128 v[64:67], v178 offset:34816
	ds_read_b128 v[236:239], v178 offset:35840
	ds_read_b128 v[240:243], v178 offset:36864
	ds_read_b128 v[244:247], v178 offset:37888
	ds_read_b128 v[248:251], v178 offset:38912
	ds_read_b128 v[184:187], v178 offset:39936
	global_load_lds_dwordx4 v[92:93], off
	v_lshl_add_u64 v[92:93], v[188:189], 0, s[52:53]
	s_mov_b32 m0, s36
	s_nop 0
	global_load_lds_dwordx4 v[92:93], off
	s_waitcnt vmcnt(8)
	s_waitcnt lgkmcnt(0)
	s_barrier
	v_mfma_f32_16x16x32_bf16 v[68:71], v[12:15], v[28:31], v[68:71]
	v_mfma_f32_16x16x32_bf16 v[140:143], v[16:19], v[32:35], v[68:71]
	v_mfma_f32_16x16x32_bf16 v[68:71], v[20:23], v[28:31], v[72:75]
	v_mfma_f32_16x16x32_bf16 v[136:139], v[24:27], v[32:35], v[68:71]
	v_mfma_f32_16x16x32_bf16 v[68:71], v[12:15], v[64:67], v[76:79]
	v_mfma_f32_16x16x32_bf16 v[112:115], v[16:19], v[236:239], v[68:71]
	v_mfma_f32_16x16x32_bf16 v[68:71], v[20:23], v[64:67], v[80:83]
	v_mfma_f32_16x16x32_bf16 v[108:111], v[24:27], v[236:239], v[68:71]
	v_mfma_f32_16x16x32_bf16 v[68:71], v[12:15], v[240:243], v[84:87]
	v_mfma_f32_16x16x32_bf16 v[96:99], v[16:19], v[244:247], v[68:71]
	v_mfma_f32_16x16x32_bf16 v[68:71], v[20:23], v[240:243], v[88:91]
	v_mfma_f32_16x16x32_bf16 v[92:95], v[24:27], v[244:247], v[68:71]
	v_mfma_f32_16x16x32_bf16 v[68:71], v[12:15], v[248:251], v[100:103]
	v_mfma_f32_16x16x32_bf16 v[80:83], v[16:19], v[184:187], v[68:71]
	v_mfma_f32_16x16x32_bf16 v[68:71], v[20:23], v[248:251], v[104:107]
	v_mfma_f32_16x16x32_bf16 v[76:79], v[24:27], v[184:187], v[68:71]
	v_mfma_f32_16x16x32_bf16 v[68:71], v[220:223], v[28:31], v[120:123]
	v_mfma_f32_16x16x32_bf16 v[28:31], v[228:231], v[28:31], v[36:39]
	v_mfma_f32_16x16x32_bf16 v[124:127], v[232:235], v[32:35], v[28:31]
	v_mfma_f32_16x16x32_bf16 v[28:31], v[220:223], v[64:67], v[40:43]
	v_mfma_f32_16x16x32_bf16 v[104:107], v[224:227], v[236:239], v[28:31]
	v_mfma_f32_16x16x32_bf16 v[28:31], v[228:231], v[64:67], v[44:47]
	v_mfma_f32_16x16x32_bf16 v[100:103], v[232:235], v[236:239], v[28:31]
	v_mfma_f32_16x16x32_bf16 v[28:31], v[220:223], v[240:243], v[48:51]
	v_mfma_f32_16x16x32_bf16 v[88:91], v[224:227], v[244:247], v[28:31]
	v_mfma_f32_16x16x32_bf16 v[28:31], v[228:231], v[240:243], v[52:55]
	v_mfma_f32_16x16x32_bf16 v[84:87], v[232:235], v[244:247], v[28:31]
	v_mfma_f32_16x16x32_bf16 v[28:31], v[220:223], v[248:251], v[56:59]
	v_mfma_f32_16x16x32_bf16 v[72:75], v[224:227], v[184:187], v[28:31]
	v_mfma_f32_16x16x32_bf16 v[28:31], v[228:231], v[248:251], v[60:63]
	v_mfma_f32_16x16x32_bf16 v[128:131], v[224:227], v[32:35], v[68:71]
	v_mfma_f32_16x16x32_bf16 v[68:71], v[232:235], v[184:187], v[28:31]
	s_barrier
	s_mov_b64 s[50:51], 0x180
	s_add_i32 s44, s44, s30
	s_nop 1
	v_lshl_add_u64 v[28:29], v[214:215], 0, s[50:51]
	s_mov_b32 m0, s44
	s_mov_b64 s[52:53], 0xb0180
	s_add_i32 s45, s44, 0x2000
	ds_read_b128 v[36:39], v178 offset:49152
	ds_read_b128 v[40:43], v178 offset:50176
	ds_read_b128 v[120:123], v178 offset:51200
	ds_read_b128 v[184:187], v178 offset:52224
	ds_read_b128 v[236:239], v178 offset:53248
	ds_read_b128 v[240:243], v178 offset:54272
	ds_read_b128 v[244:247], v178 offset:55296
	ds_read_b128 v[248:251], v178 offset:56320
	global_load_lds_dwordx4 v[28:29], off
	v_lshl_add_u64 v[28:29], v[214:215], 0, s[52:53]
	s_mov_b32 m0, s45
	s_mov_b64 s[46:47], 0x160180
	global_load_lds_dwordx4 v[28:29], off
	v_lshl_add_u64 v[28:29], v[214:215], 0, s[46:47]
	s_add_i32 s46, s48, s30
	s_mov_b32 m0, s46
	s_mov_b64 s[48:49], 0x210180
	s_add_i32 s47, s46, 0x2000
	global_load_lds_dwordx4 v[28:29], off
	v_lshl_add_u64 v[28:29], v[214:215], 0, s[48:49]
	s_mov_b32 m0, s47
	s_nop 0
	global_load_lds_dwordx4 v[28:29], off
	v_lshl_add_u64 v[28:29], v[188:189], 0, s[50:51]
	s_mov_b32 m0, s37
	s_nop 0
	global_load_lds_dwordx4 v[28:29], off
	v_lshl_add_u64 v[28:29], v[188:189], 0, s[52:53]
	s_mov_b32 m0, s38
	s_nop 0
	global_load_lds_dwordx4 v[28:29], off
	s_waitcnt vmcnt(8)
	s_waitcnt lgkmcnt(0)
	s_barrier
	v_mfma_f32_16x16x32_bf16 v[28:31], v[12:15], v[36:39], v[144:147]
	v_mfma_f32_16x16x32_bf16 v[56:59], v[16:19], v[40:43], v[28:31]
	v_mfma_f32_16x16x32_bf16 v[28:31], v[20:23], v[36:39], v[148:151]
	v_mfma_f32_16x16x32_bf16 v[52:55], v[24:27], v[40:43], v[28:31]
	v_mfma_f32_16x16x32_bf16 v[28:31], v[12:15], v[120:123], v[152:155]
	v_mfma_f32_16x16x32_bf16 v[48:51], v[16:19], v[184:187], v[28:31]
	v_mfma_f32_16x16x32_bf16 v[28:31], v[20:23], v[120:123], v[156:159]
	v_mfma_f32_16x16x32_bf16 v[44:47], v[24:27], v[184:187], v[28:31]
	v_mfma_f32_16x16x32_bf16 v[28:31], v[12:15], v[236:239], v[166:169]
	v_mfma_f32_16x16x32_bf16 v[4:7], v[12:15], v[244:247], v[4:7]
	v_mfma_f32_16x16x32_bf16 v[32:35], v[16:19], v[240:243], v[28:31]
	v_mfma_f32_16x16x32_bf16 v[28:31], v[20:23], v[236:239], v[170:173]
	v_mfma_f32_16x16x32_bf16 v[16:19], v[16:19], v[248:251], v[4:7]
	v_mfma_f32_16x16x32_bf16 v[4:7], v[20:23], v[244:247], v[8:11]
	v_mfma_f32_16x16x32_bf16 v[28:31], v[24:27], v[240:243], v[28:31]
	v_mfma_f32_16x16x32_bf16 v[12:15], v[24:27], v[248:251], v[4:7]
	v_mfma_f32_16x16x32_bf16 v[4:7], v[220:223], v[36:39], v[180:183]
	v_mfma_f32_16x16x32_bf16 v[64:67], v[224:227], v[40:43], v[4:7]
	v_mfma_f32_16x16x32_bf16 v[4:7], v[228:231], v[36:39], v[190:193]
	v_mfma_f32_16x16x32_bf16 v[60:63], v[232:235], v[40:43], v[4:7]
	v_mfma_f32_16x16x32_bf16 v[4:7], v[220:223], v[120:123], v[194:197]
	v_mfma_f32_16x16x32_bf16 v[40:43], v[224:227], v[184:187], v[4:7]
	v_mfma_f32_16x16x32_bf16 v[4:7], v[228:231], v[120:123], v[198:201]
	v_mfma_f32_16x16x32_bf16 v[36:39], v[232:235], v[184:187], v[4:7]
	v_mfma_f32_16x16x32_bf16 v[4:7], v[220:223], v[236:239], v[202:205]
	v_mfma_f32_16x16x32_bf16 v[24:27], v[224:227], v[240:243], v[4:7]
	v_mfma_f32_16x16x32_bf16 v[4:7], v[228:231], v[236:239], v[206:209]
	v_mfma_f32_16x16x32_bf16 v[20:23], v[232:235], v[240:243], v[4:7]
	v_mfma_f32_16x16x32_bf16 v[4:7], v[220:223], v[244:247], v[216:219]
	v_mfma_f32_16x16x32_bf16 v[8:11], v[224:227], v[248:251], v[4:7]
	v_mfma_f32_16x16x32_bf16 v[4:7], v[228:231], v[244:247], v[132:135]
	v_mfma_f32_16x16x32_bf16 v[4:7], v[232:235], v[248:251], v[4:7]
	s_barrier
	s_add_u32 s26, s26, 0x160180
	s_addc_u32 s27, s27, 0
	s_add_u32 s24, s24, 0x200
	s_addc_u32 s25, s25, 0
	s_mov_b32 s48, 0
	s_mov_b64 s[54:55], 0x160000
	s_mov_b64 s[56:57], 0x210000
	s_mov_b64 s[60:61], 0xb0080
	.p2align	6

.LBB0_323:
	s_ashr_i32 s23, s22, 31
	s_lshl_b64 s[4:5], s[22:23], 20
	v_readlane_b32 s26, v254, 18
	v_readlane_b32 s27, v254, 19
	s_add_u32 s26, s26, s4
	s_addc_u32 s27, s27, s5
	s_add_i32 s28, 0, 0x10000
	s_add_i32 s33, 0, 0x14000
	v_add_u32_e32 v132, s28, v197
	s_waitcnt lgkmcnt(0)
	v_add_u32_e32 v133, s33, v197
	ds_read_b128 v[4:7], v132
	ds_read_b128 v[8:11], v132 offset:1024
	ds_read_b128 v[12:15], v132 offset:2048
	ds_read_b128 v[16:19], v132 offset:3072
	ds_read_b128 v[20:23], v133
	ds_read_b128 v[24:27], v133 offset:1024
	ds_read_b128 v[28:31], v133 offset:2048
	ds_read_b128 v[32:35], v133 offset:3072
	s_and_b64 s[4:5], s[10:11], exec
	s_cselect_b32 s3, s27, s13
	s_cselect_b32 s4, s26, s12
	v_lshl_add_u64 v[194:195], s[14:15], 0, v[166:167]
	s_mov_b64 s[10:11], 0x84080
	s_add_i32 s5, s30, 0xc000
	v_lshl_add_u64 v[68:69], v[194:195], 0, s[10:11]
	s_mov_b32 m0, s5
	s_mov_b64 s[10:11], 0xc6080
	s_add_i32 s23, s30, 0xe000
	ds_read_b128 v[36:39], v200
	ds_read_b128 v[40:43], v200 offset:1024
	ds_read_b128 v[44:47], v200 offset:2048
	ds_read_b128 v[48:51], v200 offset:3072
	ds_read_b128 v[52:55], v200 offset:4096
	ds_read_b128 v[56:59], v200 offset:5120
	ds_read_b128 v[60:63], v200 offset:6144
	ds_read_b128 v[64:67], v200 offset:7168
	global_load_lds_dwordx4 v[68:69], off
	v_lshl_add_u64 v[68:69], v[194:195], 0, s[10:11]
	s_mov_b32 m0, s23
	s_nop 0
	global_load_lds_dwordx4 v[68:69], off
	s_waitcnt vmcnt(16)
	s_waitcnt lgkmcnt(0)
	s_barrier
	v_mfma_f32_16x16x32_bf16 v[88:91], v[12:15], v[52:55], 0
	v_mfma_f32_16x16x32_bf16 v[92:95], v[16:19], v[56:59], v[88:91]
	v_mfma_f32_16x16x32_bf16 v[88:91], v[4:7], v[60:63], 0
	v_mfma_f32_16x16x32_bf16 v[68:71], v[4:7], v[36:39], 0
	v_mfma_f32_16x16x32_bf16 v[72:75], v[12:15], v[36:39], 0
	v_mfma_f32_16x16x32_bf16 v[76:79], v[4:7], v[44:47], 0
	v_mfma_f32_16x16x32_bf16 v[80:83], v[12:15], v[44:47], 0
	v_mfma_f32_16x16x32_bf16 v[84:87], v[4:7], v[52:55], 0
	v_mfma_f32_16x16x32_bf16 v[96:99], v[8:11], v[64:67], v[88:91]
	v_mfma_f32_16x16x32_bf16 v[88:91], v[12:15], v[60:63], 0
	v_mfma_f32_16x16x32_bf16 v[68:71], v[8:11], v[40:43], v[68:71]
	v_mfma_f32_16x16x32_bf16 v[72:75], v[16:19], v[40:43], v[72:75]
	v_mfma_f32_16x16x32_bf16 v[76:79], v[8:11], v[48:51], v[76:79]
	v_mfma_f32_16x16x32_bf16 v[80:83], v[16:19], v[48:51], v[80:83]
	v_mfma_f32_16x16x32_bf16 v[84:87], v[8:11], v[56:59], v[84:87]
	v_mfma_f32_16x16x32_bf16 v[108:111], v[16:19], v[64:67], v[88:91]
	v_mfma_f32_16x16x32_bf16 v[88:91], v[20:23], v[36:39], 0
	v_mfma_f32_16x16x32_bf16 v[36:39], v[28:31], v[36:39], 0
	v_mfma_f32_16x16x32_bf16 v[112:115], v[24:27], v[40:43], v[88:91]
	v_mfma_f32_16x16x32_bf16 v[36:39], v[32:35], v[40:43], v[36:39]
	v_mfma_f32_16x16x32_bf16 v[40:43], v[20:23], v[44:47], 0
	v_mfma_f32_16x16x32_bf16 v[44:47], v[28:31], v[44:47], 0
	v_mfma_f32_16x16x32_bf16 v[40:43], v[24:27], v[48:51], v[40:43]
	v_mfma_f32_16x16x32_bf16 v[44:47], v[32:35], v[48:51], v[44:47]
	v_mfma_f32_16x16x32_bf16 v[48:51], v[20:23], v[52:55], 0
	v_mfma_f32_16x16x32_bf16 v[52:55], v[28:31], v[52:55], 0
	v_mfma_f32_16x16x32_bf16 v[48:51], v[24:27], v[56:59], v[48:51]
	v_mfma_f32_16x16x32_bf16 v[52:55], v[32:35], v[56:59], v[52:55]
	v_mfma_f32_16x16x32_bf16 v[56:59], v[20:23], v[60:63], 0
	v_mfma_f32_16x16x32_bf16 v[60:63], v[28:31], v[60:63], 0
	v_mfma_f32_16x16x32_bf16 v[56:59], v[24:27], v[64:67], v[56:59]
	v_mfma_f32_16x16x32_bf16 v[60:63], v[32:35], v[64:67], v[60:63]
	s_barrier
	v_lshl_add_u64 v[214:215], s[12:13], 0, v[164:165]
	s_mov_b64 s[10:11], 0x100
	s_add_i32 s28, s28, s0
	v_lshl_add_u64 v[134:135], v[214:215], 0, s[10:11]
	s_mov_b32 m0, s28
	s_mov_b64 s[46:47], 0x40100
	s_add_i32 s29, s28, 0x2000
	ds_read_b128 v[64:67], v200 offset:16384
	ds_read_b128 v[88:91], v200 offset:17408
	ds_read_b128 v[100:103], v200 offset:18432
	ds_read_b128 v[104:107], v200 offset:19456
	ds_read_b128 v[116:119], v200 offset:20480
	ds_read_b128 v[120:123], v200 offset:21504
	ds_read_b128 v[124:127], v200 offset:22528
	ds_read_b128 v[128:131], v200 offset:23552
	global_load_lds_dwordx4 v[134:135], off
	v_lshl_add_u64 v[134:135], v[214:215], 0, s[46:47]
	s_mov_b32 m0, s29
	s_mov_b64 s[46:47], 0x80100
	s_add_i32 s33, s33, s0
	global_load_lds_dwordx4 v[134:135], off
	v_lshl_add_u64 v[134:135], v[214:215], 0, s[46:47]
	s_mov_b32 m0, s33
	s_mov_b64 s[46:47], 0xc0100
	s_add_i32 s45, s33, 0x2000
	global_load_lds_dwordx4 v[134:135], off
	v_lshl_add_u64 v[134:135], v[214:215], 0, s[46:47]
	s_mov_b32 m0, s45
	s_nop 0
	global_load_lds_dwordx4 v[134:135], off
	v_lshl_add_u64 v[134:135], v[194:195], 0, s[10:11]
	s_mov_b32 m0, s30
	s_mov_b64 s[10:11], 0x42100
	global_load_lds_dwordx4 v[134:135], off
	v_lshl_add_u64 v[134:135], v[194:195], 0, s[10:11]
	s_mov_b32 m0, s31
	s_nop 0
	global_load_lds_dwordx4 v[134:135], off
	s_waitcnt vmcnt(16)
	s_waitcnt lgkmcnt(0)
	s_barrier
	v_mfma_f32_16x16x32_bf16 v[134:137], v[4:7], v[64:67], 0
	v_mfma_f32_16x16x32_bf16 v[144:147], v[4:7], v[100:103], 0
	v_mfma_f32_16x16x32_bf16 v[152:155], v[4:7], v[116:119], 0
	v_mfma_f32_16x16x32_bf16 v[4:7], v[4:7], v[124:127], 0
	v_mfma_f32_16x16x32_bf16 v[136:139], v[8:11], v[88:91], v[134:137]
	v_mfma_f32_16x16x32_bf16 v[144:147], v[8:11], v[104:107], v[144:147]
	v_mfma_f32_16x16x32_bf16 v[152:155], v[8:11], v[120:123], v[152:155]
	v_mfma_f32_16x16x32_bf16 v[4:7], v[8:11], v[128:131], v[4:7]
	v_mfma_f32_16x16x32_bf16 v[8:11], v[12:15], v[124:127], 0
	v_mfma_f32_16x16x32_bf16 v[140:143], v[12:15], v[64:67], 0
	v_mfma_f32_16x16x32_bf16 v[148:151], v[12:15], v[100:103], 0
	v_mfma_f32_16x16x32_bf16 v[156:159], v[12:15], v[116:119], 0
	v_mfma_f32_16x16x32_bf16 v[12:15], v[16:19], v[128:131], v[8:11]
	v_mfma_f32_16x16x32_bf16 v[140:143], v[16:19], v[88:91], v[140:143]
	v_mfma_f32_16x16x32_bf16 v[148:151], v[16:19], v[104:107], v[148:151]
	v_mfma_f32_16x16x32_bf16 v[156:159], v[16:19], v[120:123], v[156:159]
	v_mfma_f32_16x16x32_bf16 v[8:11], v[20:23], v[64:67], 0
	v_mfma_f32_16x16x32_bf16 v[16:19], v[24:27], v[88:91], v[8:11]
	v_mfma_f32_16x16x32_bf16 v[8:11], v[28:31], v[64:67], 0
	v_mfma_f32_16x16x32_bf16 v[160:163], v[32:35], v[88:91], v[8:11]
	v_mfma_f32_16x16x32_bf16 v[8:11], v[20:23], v[100:103], 0
	v_mfma_f32_16x16x32_bf16 v[174:177], v[24:27], v[104:107], v[8:11]
	v_mfma_f32_16x16x32_bf16 v[8:11], v[28:31], v[100:103], 0
	v_mfma_f32_16x16x32_bf16 v[178:181], v[32:35], v[104:107], v[8:11]
	v_mfma_f32_16x16x32_bf16 v[8:11], v[20:23], v[116:119], 0
	v_mfma_f32_16x16x32_bf16 v[182:185], v[24:27], v[120:123], v[8:11]
	v_mfma_f32_16x16x32_bf16 v[8:11], v[28:31], v[116:119], 0
	v_mfma_f32_16x16x32_bf16 v[190:193], v[32:35], v[120:123], v[8:11]
	v_mfma_f32_16x16x32_bf16 v[8:11], v[20:23], v[124:127], 0
	v_mfma_f32_16x16x32_bf16 v[202:205], v[24:27], v[128:131], v[8:11]
	v_mfma_f32_16x16x32_bf16 v[8:11], v[28:31], v[124:127], 0
	v_mfma_f32_16x16x32_bf16 v[206:209], v[32:35], v[128:131], v[8:11]
	s_barrier
	s_add_i32 s46, 0, 0x18000
	s_add_i32 s48, 0, 0x1c000
	v_add_u32_e32 v134, s46, v197
	v_add_u32_e32 v135, s48, v197
	s_nop 0
	ds_read_b128 v[8:11], v134
	ds_read_b128 v[28:31], v134 offset:1024
	ds_read_b128 v[32:35], v134 offset:2048
	ds_read_b128 v[64:67], v134 offset:3072
	ds_read_b128 v[216:219], v135
	ds_read_b128 v[220:223], v135 offset:1024
	ds_read_b128 v[224:227], v135 offset:2048
	ds_read_b128 v[228:231], v135 offset:3072
	s_mov_b64 s[10:11], 0x84100
	s_mov_b32 m0, s34
	v_lshl_add_u64 v[88:89], v[194:195], 0, s[10:11]
	s_mov_b64 s[10:11], 0xc6100
	ds_read_b128 v[20:23], v200 offset:32768
	ds_read_b128 v[24:27], v200 offset:33792
	ds_read_b128 v[232:235], v200 offset:34816
	ds_read_b128 v[236:239], v200 offset:35840
	ds_read_b128 v[240:243], v200 offset:36864
	ds_read_b128 v[244:247], v200 offset:37888
	ds_read_b128 v[248:251], v200 offset:38912
	ds_read_b128 v[186:189], v200 offset:39936
	global_load_lds_dwordx4 v[88:89], off
	v_lshl_add_u64 v[88:89], v[194:195], 0, s[10:11]
	s_mov_b32 m0, s35
	s_nop 0
	global_load_lds_dwordx4 v[88:89], off
	s_waitcnt vmcnt(8)
	s_waitcnt lgkmcnt(0)
	s_barrier
	v_mfma_f32_16x16x32_bf16 v[68:71], v[8:11], v[20:23], v[68:71]
	v_mfma_f32_16x16x32_bf16 v[120:123], v[28:31], v[24:27], v[68:71]
	v_mfma_f32_16x16x32_bf16 v[68:71], v[32:35], v[20:23], v[72:75]
	v_mfma_f32_16x16x32_bf16 v[116:119], v[64:67], v[24:27], v[68:71]
	v_mfma_f32_16x16x32_bf16 v[68:71], v[8:11], v[232:235], v[76:79]
	v_mfma_f32_16x16x32_bf16 v[104:107], v[28:31], v[236:239], v[68:71]
	v_mfma_f32_16x16x32_bf16 v[68:71], v[32:35], v[232:235], v[80:83]
	v_mfma_f32_16x16x32_bf16 v[100:103], v[64:67], v[236:239], v[68:71]
	v_mfma_f32_16x16x32_bf16 v[68:71], v[8:11], v[240:243], v[84:87]
	v_mfma_f32_16x16x32_bf16 v[88:91], v[28:31], v[244:247], v[68:71]
	v_mfma_f32_16x16x32_bf16 v[68:71], v[32:35], v[240:243], v[92:95]
	v_mfma_f32_16x16x32_bf16 v[84:87], v[64:67], v[244:247], v[68:71]
	v_mfma_f32_16x16x32_bf16 v[68:71], v[8:11], v[248:251], v[96:99]
	v_mfma_f32_16x16x32_bf16 v[72:75], v[28:31], v[186:189], v[68:71]
	v_mfma_f32_16x16x32_bf16 v[68:71], v[32:35], v[248:251], v[108:111]
	v_mfma_f32_16x16x32_bf16 v[68:71], v[64:67], v[186:189], v[68:71]
	v_mfma_f32_16x16x32_bf16 v[76:79], v[216:219], v[20:23], v[112:115]
	v_mfma_f32_16x16x32_bf16 v[20:23], v[224:227], v[20:23], v[36:39]
	v_mfma_f32_16x16x32_bf16 v[124:127], v[228:231], v[24:27], v[20:23]
	v_mfma_f32_16x16x32_bf16 v[20:23], v[216:219], v[232:235], v[40:43]
	v_mfma_f32_16x16x32_bf16 v[112:115], v[220:223], v[236:239], v[20:23]
	v_mfma_f32_16x16x32_bf16 v[20:23], v[224:227], v[232:235], v[44:47]
	v_mfma_f32_16x16x32_bf16 v[108:111], v[228:231], v[236:239], v[20:23]
	v_mfma_f32_16x16x32_bf16 v[20:23], v[216:219], v[240:243], v[48:51]
	v_mfma_f32_16x16x32_bf16 v[96:99], v[220:223], v[244:247], v[20:23]
	v_mfma_f32_16x16x32_bf16 v[20:23], v[224:227], v[240:243], v[52:55]
	v_mfma_f32_16x16x32_bf16 v[92:95], v[228:231], v[244:247], v[20:23]
	v_mfma_f32_16x16x32_bf16 v[20:23], v[216:219], v[248:251], v[56:59]
	v_mfma_f32_16x16x32_bf16 v[80:83], v[220:223], v[186:189], v[20:23]
	v_mfma_f32_16x16x32_bf16 v[20:23], v[224:227], v[248:251], v[60:63]
	v_mfma_f32_16x16x32_bf16 v[128:131], v[220:223], v[24:27], v[76:79]
	v_mfma_f32_16x16x32_bf16 v[76:79], v[228:231], v[186:189], v[20:23]
	s_barrier
; #define PG8_MMA(ai, bj, At, Bt) do { __builtin_amdgcn_s_setprio(1); _Pragma("unroll") for (int m = 0; m < 4; ++m) _Pragma("unroll") for (int n = 0; n < 2; ++n) _Pragma("unroll") for (int k = 0; k < 2; ++k) \
;         acc[ai][bj][m][n] = __builtin_amdgcn_mfma_f32_16x16x32_bf16(Bt[n][k], At[m][k], acc[ai][bj][m][n], 0, 0, 0); __builtin_amdgcn_s_setprio(0); } while (0)
; #define PG8_WAIT_V(n) asm volatile("s_waitcnt vmcnt(" #n ")" ::: "memory")
; #define PG8_TRIP_HEAD(T) const int t = (T); const bool last = (t == nt - 2); \
;             const char* a1 = cA + (size_t)(t + 1) * kstep; \
;             const char* a2 = last ? nA : cA + (size_t)(t + 2) * kstep; const char* b2 = last ? nB : cB + (size_t)(t + 2) * kstep; \
;             const char* a3 = a2 + kstep; const char* b3 = b2 + kstep; \
;             if (last && has_next) S.a_ready(nxt);
; template <class Epi, class Sched, bool ALIGN_EPI = false, bool SP2 = false>
; __device__ __forceinline__ void gemm_phase(PG8_LAS unsigned char* lds, const Gemm g, const Sched& S, const Epi& E) {
;     ...
;         if constexpr (SP2) {
;             { PG8_TRIP_HEAD(0) PG8_TRIP_SP2(asm volatile("s_waitcnt vmcnt(%0)" :: "n"(8 + Epi::NST) : "memory"), PG8_MMAZ) }
;             for (int tt = 2; tt < nt; tt += 2) { PG8_TRIP_HEAD(tt) PG8_TRIP_SP2(PG8_WAIT_V(8), PG8_MMA) }
	s_mov_b64 s[10:11], 0x180
	s_add_i32 s46, s46, s0
	s_nop 1
	v_lshl_add_u64 v[20:21], v[214:215], 0, s[10:11]
	s_mov_b32 m0, s46
	s_mov_b64 s[50:51], 0x40180
	s_add_i32 s47, s46, 0x2000
	ds_read_b128 v[44:47], v200 offset:49152
	ds_read_b128 v[48:51], v200 offset:50176
	ds_read_b128 v[186:189], v200 offset:51200
	ds_read_b128 v[232:235], v200 offset:52224
	ds_read_b128 v[236:239], v200 offset:53248
	ds_read_b128 v[240:243], v200 offset:54272
	ds_read_b128 v[244:247], v200 offset:55296
	ds_read_b128 v[248:251], v200 offset:56320
	global_load_lds_dwordx4 v[20:21], off
	v_lshl_add_u64 v[20:21], v[214:215], 0, s[50:51]
	s_mov_b32 m0, s47
	s_mov_b64 s[50:51], 0x80180
	s_add_i32 s48, s48, s0
	global_load_lds_dwordx4 v[20:21], off
	v_lshl_add_u64 v[20:21], v[214:215], 0, s[50:51]
	s_mov_b32 m0, s48
	s_mov_b64 s[50:51], 0xc0180
	s_add_i32 s49, s48, 0x2000
	global_load_lds_dwordx4 v[20:21], off
	v_lshl_add_u64 v[20:21], v[214:215], 0, s[50:51]
	s_mov_b32 m0, s49
	s_nop 0
	global_load_lds_dwordx4 v[20:21], off
	v_lshl_add_u64 v[20:21], v[194:195], 0, s[10:11]
	s_mov_b32 m0, s38
	s_mov_b64 s[10:11], 0x42180
	global_load_lds_dwordx4 v[20:21], off
	v_lshl_add_u64 v[20:21], v[194:195], 0, s[10:11]
	s_mov_b32 m0, s39
	s_nop 0
	global_load_lds_dwordx4 v[20:21], off
	s_waitcnt vmcnt(8)
	s_waitcnt lgkmcnt(0)
	s_barrier
	v_mfma_f32_16x16x32_bf16 v[20:23], v[8:11], v[44:47], v[136:139]
	v_mfma_f32_16x16x32_bf16 v[56:59], v[28:31], v[48:51], v[20:23]
	v_mfma_f32_16x16x32_bf16 v[20:23], v[32:35], v[44:47], v[140:143]
	v_mfma_f32_16x16x32_bf16 v[52:55], v[64:67], v[48:51], v[20:23]
	v_mfma_f32_16x16x32_bf16 v[20:23], v[8:11], v[186:189], v[144:147]
	v_mfma_f32_16x16x32_bf16 v[40:43], v[28:31], v[232:235], v[20:23]
	v_mfma_f32_16x16x32_bf16 v[20:23], v[32:35], v[186:189], v[148:151]
	v_mfma_f32_16x16x32_bf16 v[36:39], v[64:67], v[232:235], v[20:23]
	v_mfma_f32_16x16x32_bf16 v[20:23], v[8:11], v[236:239], v[152:155]
	v_mfma_f32_16x16x32_bf16 v[4:7], v[8:11], v[244:247], v[4:7]
	v_mfma_f32_16x16x32_bf16 v[24:27], v[28:31], v[240:243], v[20:23]
	v_mfma_f32_16x16x32_bf16 v[20:23], v[32:35], v[236:239], v[156:159]
	v_mfma_f32_16x16x32_bf16 v[8:11], v[28:31], v[248:251], v[4:7]
	v_mfma_f32_16x16x32_bf16 v[4:7], v[32:35], v[244:247], v[12:15]
	v_mfma_f32_16x16x32_bf16 v[20:23], v[64:67], v[240:243], v[20:23]
	v_mfma_f32_16x16x32_bf16 v[4:7], v[64:67], v[248:251], v[4:7]
	v_mfma_f32_16x16x32_bf16 v[12:15], v[216:219], v[44:47], v[16:19]
	v_mfma_f32_16x16x32_bf16 v[64:67], v[220:223], v[48:51], v[12:15]
	v_mfma_f32_16x16x32_bf16 v[12:15], v[224:227], v[44:47], v[160:163]
	v_mfma_f32_16x16x32_bf16 v[60:63], v[228:231], v[48:51], v[12:15]
	v_mfma_f32_16x16x32_bf16 v[12:15], v[216:219], v[186:189], v[174:177]
	v_mfma_f32_16x16x32_bf16 v[48:51], v[220:223], v[232:235], v[12:15]
	v_mfma_f32_16x16x32_bf16 v[12:15], v[224:227], v[186:189], v[178:181]
	v_mfma_f32_16x16x32_bf16 v[44:47], v[228:231], v[232:235], v[12:15]
	v_mfma_f32_16x16x32_bf16 v[12:15], v[216:219], v[236:239], v[182:185]
	v_mfma_f32_16x16x32_bf16 v[32:35], v[220:223], v[240:243], v[12:15]
	v_mfma_f32_16x16x32_bf16 v[12:15], v[224:227], v[236:239], v[190:193]
	v_mfma_f32_16x16x32_bf16 v[28:31], v[228:231], v[240:243], v[12:15]
	v_mfma_f32_16x16x32_bf16 v[12:15], v[216:219], v[244:247], v[202:205]
	v_mfma_f32_16x16x32_bf16 v[16:19], v[220:223], v[248:251], v[12:15]
	v_mfma_f32_16x16x32_bf16 v[12:15], v[224:227], v[244:247], v[206:209]
	v_mfma_f32_16x16x32_bf16 v[12:15], v[228:231], v[248:251], v[12:15]
	s_barrier
	s_add_u32 s10, s14, 0x84180
	s_addc_u32 s11, s15, 0
	s_add_u32 s12, s12, 0x200
	s_addc_u32 s13, s13, 0
	s_mov_b32 s14, 0
	s_mov_b64 s[54:55], 0x80000
	s_mov_b64 s[56:57], 0x80080
	s_mov_b64 s[60:61], 0xc0000
	s_mov_b64 s[62:63], 0xc0080
	s_mov_b64 s[64:65], 0xc6000
	.p2align	6

.LBB0_593:
	v_readlane_b32 s18, v253, 7
	v_readlane_b32 s34, v254, 59
	s_cmp_eq_u32 s29, 0
	v_readlane_b32 s19, v253, 8
	v_readlane_b32 s35, v254, 60
	s_cselect_b32 s33, s35, s19
	s_cselect_b32 s34, s34, s18
	s_ashr_i32 s15, s14, 31
	s_lshl_b64 s[18:19], s[14:15], 20
	s_add_u32 s18, s34, s18
	s_addc_u32 s19, s33, s19
	s_and_b64 s[4:5], s[4:5], exec
	s_cselect_b32 s4, s19, s9
	s_cselect_b32 s5, s18, s8
	s_add_i32 s35, 0, 0x10000
	s_add_i32 s37, 0, 0x14000
	v_add_u32_e32 v116, s35, v219
	v_add_u32_e32 v117, s37, v219
	ds_read_b128 v[4:7], v116
	ds_read_b128 v[8:11], v116 offset:1024
	ds_read_b128 v[12:15], v116 offset:2048
	ds_read_b128 v[16:19], v116 offset:3072
	ds_read_b128 v[20:23], v117
	ds_read_b128 v[24:27], v117 offset:1024
	ds_read_b128 v[28:31], v117 offset:2048
	ds_read_b128 v[32:35], v117 offset:3072
	s_mov_b32 s15, 0
	v_lshl_add_u64 v[192:193], s[20:21], 0, v[196:197]
	s_mov_b64 s[38:39], 0x84080
	s_add_i32 s33, s23, 0xc000
	v_lshl_add_u64 v[68:69], v[192:193], 0, s[38:39]
	s_mov_b32 m0, s33
	s_mov_b64 s[38:39], 0xc6080
	s_add_i32 s34, s23, 0xe000
	ds_read_b128 v[36:39], v221
	ds_read_b128 v[40:43], v221 offset:1024
	ds_read_b128 v[44:47], v221 offset:2048
	ds_read_b128 v[48:51], v221 offset:3072
	ds_read_b128 v[52:55], v221 offset:4096
	ds_read_b128 v[56:59], v221 offset:5120
	ds_read_b128 v[60:63], v221 offset:6144
	ds_read_b128 v[64:67], v221 offset:7168
	global_load_lds_dwordx4 v[68:69], off
	v_lshl_add_u64 v[68:69], v[192:193], 0, s[38:39]
	s_mov_b32 m0, s34
	s_nop 0
	global_load_lds_dwordx4 v[68:69], off
	s_waitcnt vmcnt(8)
	s_waitcnt lgkmcnt(0)
	s_barrier
	v_mfma_f32_16x16x32_bf16 v[92:95], v[4:7], v[60:63], 0
	v_mfma_f32_16x16x32_bf16 v[68:71], v[4:7], v[36:39], 0
	v_mfma_f32_16x16x32_bf16 v[72:75], v[12:15], v[36:39], 0
	v_mfma_f32_16x16x32_bf16 v[76:79], v[4:7], v[44:47], 0
	v_mfma_f32_16x16x32_bf16 v[80:83], v[12:15], v[44:47], 0
	v_mfma_f32_16x16x32_bf16 v[84:87], v[4:7], v[52:55], 0
	v_mfma_f32_16x16x32_bf16 v[88:91], v[12:15], v[52:55], 0
	v_mfma_f32_16x16x32_bf16 v[100:103], v[8:11], v[64:67], v[92:95]
	v_mfma_f32_16x16x32_bf16 v[92:95], v[12:15], v[60:63], 0
	v_mfma_f32_16x16x32_bf16 v[68:71], v[8:11], v[40:43], v[68:71]
	v_mfma_f32_16x16x32_bf16 v[72:75], v[16:19], v[40:43], v[72:75]
	v_mfma_f32_16x16x32_bf16 v[76:79], v[8:11], v[48:51], v[76:79]
	v_mfma_f32_16x16x32_bf16 v[80:83], v[16:19], v[48:51], v[80:83]
	v_mfma_f32_16x16x32_bf16 v[84:87], v[8:11], v[56:59], v[84:87]
	v_mfma_f32_16x16x32_bf16 v[88:91], v[16:19], v[56:59], v[88:91]
	v_mfma_f32_16x16x32_bf16 v[104:107], v[16:19], v[64:67], v[92:95]
	v_mfma_f32_16x16x32_bf16 v[92:95], v[20:23], v[36:39], 0
	v_mfma_f32_16x16x32_bf16 v[36:39], v[28:31], v[36:39], 0
	v_mfma_f32_16x16x32_bf16 v[118:121], v[24:27], v[40:43], v[92:95]
	v_mfma_f32_16x16x32_bf16 v[36:39], v[32:35], v[40:43], v[36:39]
	v_mfma_f32_16x16x32_bf16 v[40:43], v[20:23], v[44:47], 0
	v_mfma_f32_16x16x32_bf16 v[44:47], v[28:31], v[44:47], 0
	v_mfma_f32_16x16x32_bf16 v[40:43], v[24:27], v[48:51], v[40:43]
	v_mfma_f32_16x16x32_bf16 v[44:47], v[32:35], v[48:51], v[44:47]
	v_mfma_f32_16x16x32_bf16 v[48:51], v[20:23], v[52:55], 0
	v_mfma_f32_16x16x32_bf16 v[52:55], v[28:31], v[52:55], 0
	v_mfma_f32_16x16x32_bf16 v[48:51], v[24:27], v[56:59], v[48:51]
	v_mfma_f32_16x16x32_bf16 v[52:55], v[32:35], v[56:59], v[52:55]
	v_mfma_f32_16x16x32_bf16 v[56:59], v[20:23], v[60:63], 0
	v_mfma_f32_16x16x32_bf16 v[60:63], v[28:31], v[60:63], 0
	v_mfma_f32_16x16x32_bf16 v[56:59], v[24:27], v[64:67], v[56:59]
	v_mfma_f32_16x16x32_bf16 v[60:63], v[32:35], v[64:67], v[60:63]
	s_barrier
	v_lshl_add_u64 v[250:251], s[8:9], 0, v[194:195]
	s_mov_b64 s[40:41], 0x100
	s_add_i32 s35, s35, s22
	v_lshl_add_u64 v[134:135], v[250:251], 0, s[40:41]
	s_mov_b32 m0, s35
	s_mov_b64 s[38:39], 0x40100
	s_add_i32 s36, s35, 0x2000
	ds_read_b128 v[64:67], v221 offset:16384
	ds_read_b128 v[92:95], v221 offset:17408
	ds_read_b128 v[96:99], v221 offset:18432
	ds_read_b128 v[108:111], v221 offset:19456
	ds_read_b128 v[112:115], v221 offset:20480
	ds_read_b128 v[122:125], v221 offset:21504
	ds_read_b128 v[126:129], v221 offset:22528
	ds_read_b128 v[130:133], v221 offset:23552
	global_load_lds_dwordx4 v[134:135], off
	v_lshl_add_u64 v[134:135], v[250:251], 0, s[38:39]
	s_mov_b32 m0, s36
	s_mov_b64 s[38:39], 0x80100
	s_add_i32 s37, s37, s22
	global_load_lds_dwordx4 v[134:135], off
	v_lshl_add_u64 v[134:135], v[250:251], 0, s[38:39]
	s_mov_b32 m0, s37
	s_mov_b64 s[38:39], 0xc0100
	global_load_lds_dwordx4 v[134:135], off
	v_lshl_add_u64 v[134:135], v[250:251], 0, s[38:39]
	s_add_i32 s38, s37, 0x2000
	s_mov_b32 m0, s38
	s_nop 0
	global_load_lds_dwordx4 v[134:135], off
	v_lshl_add_u64 v[134:135], v[192:193], 0, s[40:41]
	s_mov_b32 m0, s23
	s_mov_b64 s[40:41], 0x42100
	global_load_lds_dwordx4 v[134:135], off
	v_lshl_add_u64 v[134:135], v[192:193], 0, s[40:41]
	s_mov_b32 m0, s24
	s_nop 0
	global_load_lds_dwordx4 v[134:135], off
	s_waitcnt vmcnt(8)
	s_waitcnt lgkmcnt(0)
	s_barrier
	v_mfma_f32_16x16x32_bf16 v[134:137], v[4:7], v[64:67], 0
	v_mfma_f32_16x16x32_bf16 v[144:147], v[4:7], v[96:99], 0
	v_mfma_f32_16x16x32_bf16 v[152:155], v[4:7], v[112:115], 0
	v_mfma_f32_16x16x32_bf16 v[4:7], v[4:7], v[126:129], 0
	v_mfma_f32_16x16x32_bf16 v[136:139], v[8:11], v[92:95], v[134:137]
	v_mfma_f32_16x16x32_bf16 v[144:147], v[8:11], v[108:111], v[144:147]
	v_mfma_f32_16x16x32_bf16 v[152:155], v[8:11], v[122:125], v[152:155]
	v_mfma_f32_16x16x32_bf16 v[4:7], v[8:11], v[130:133], v[4:7]
	v_mfma_f32_16x16x32_bf16 v[8:11], v[12:15], v[126:129], 0
	v_mfma_f32_16x16x32_bf16 v[140:143], v[12:15], v[64:67], 0
	v_mfma_f32_16x16x32_bf16 v[148:151], v[12:15], v[96:99], 0
	v_mfma_f32_16x16x32_bf16 v[156:159], v[12:15], v[112:115], 0
	v_mfma_f32_16x16x32_bf16 v[8:11], v[16:19], v[130:133], v[8:11]
	v_mfma_f32_16x16x32_bf16 v[140:143], v[16:19], v[92:95], v[140:143]
	v_mfma_f32_16x16x32_bf16 v[148:151], v[16:19], v[108:111], v[148:151]
	v_mfma_f32_16x16x32_bf16 v[156:159], v[16:19], v[122:125], v[156:159]
	v_mfma_f32_16x16x32_bf16 v[12:15], v[20:23], v[64:67], 0
	v_mfma_f32_16x16x32_bf16 v[160:163], v[24:27], v[92:95], v[12:15]
	v_mfma_f32_16x16x32_bf16 v[12:15], v[28:31], v[64:67], 0
	v_mfma_f32_16x16x32_bf16 v[164:167], v[32:35], v[92:95], v[12:15]
	v_mfma_f32_16x16x32_bf16 v[12:15], v[20:23], v[96:99], 0
	v_mfma_f32_16x16x32_bf16 v[168:171], v[24:27], v[108:111], v[12:15]
	v_mfma_f32_16x16x32_bf16 v[12:15], v[28:31], v[96:99], 0
	v_mfma_f32_16x16x32_bf16 v[172:175], v[32:35], v[108:111], v[12:15]
	v_mfma_f32_16x16x32_bf16 v[12:15], v[20:23], v[112:115], 0
	v_mfma_f32_16x16x32_bf16 v[176:179], v[24:27], v[122:125], v[12:15]
	v_mfma_f32_16x16x32_bf16 v[12:15], v[28:31], v[112:115], 0
	v_mfma_f32_16x16x32_bf16 v[180:183], v[32:35], v[122:125], v[12:15]
	v_mfma_f32_16x16x32_bf16 v[12:15], v[20:23], v[126:129], 0
	v_mfma_f32_16x16x32_bf16 v[184:187], v[24:27], v[130:133], v[12:15]
	v_mfma_f32_16x16x32_bf16 v[12:15], v[28:31], v[126:129], 0
	v_mfma_f32_16x16x32_bf16 v[188:191], v[32:35], v[130:133], v[12:15]
	s_barrier
	s_add_i32 s39, 0, 0x18000
	s_add_i32 s41, 0, 0x1c000
	v_add_u32_e32 v134, s39, v219
	v_add_u32_e32 v135, s41, v219
	s_nop 0
	ds_read_b128 v[12:15], v134
	ds_read_b128 v[16:19], v134 offset:1024
	ds_read_b128 v[20:23], v134 offset:2048
	ds_read_b128 v[24:27], v134 offset:3072
	ds_read_b128 v[202:205], v135
	ds_read_b128 v[206:209], v135 offset:1024
	ds_read_b128 v[222:225], v135 offset:2048
	ds_read_b128 v[226:229], v135 offset:3072
	s_mov_b64 s[42:43], 0x84100
	s_mov_b32 m0, s25
	v_lshl_add_u64 v[92:93], v[192:193], 0, s[42:43]
	s_mov_b64 s[42:43], 0xc6100
	ds_read_b128 v[28:31], v221 offset:32768
	ds_read_b128 v[32:35], v221 offset:33792
	ds_read_b128 v[64:67], v221 offset:34816
	ds_read_b128 v[230:233], v221 offset:35840
	ds_read_b128 v[234:237], v221 offset:36864
	ds_read_b128 v[238:241], v221 offset:37888
	ds_read_b128 v[242:245], v221 offset:38912
	ds_read_b128 v[246:249], v221 offset:39936
	global_load_lds_dwordx4 v[92:93], off
	v_lshl_add_u64 v[92:93], v[192:193], 0, s[42:43]
	s_mov_b32 m0, s26
	s_nop 0
	global_load_lds_dwordx4 v[92:93], off
	s_waitcnt vmcnt(8)
	s_waitcnt lgkmcnt(0)
	s_barrier
	v_mfma_f32_16x16x32_bf16 v[68:71], v[12:15], v[28:31], v[68:71]
	v_mfma_f32_16x16x32_bf16 v[130:133], v[16:19], v[32:35], v[68:71]
	v_mfma_f32_16x16x32_bf16 v[68:71], v[20:23], v[28:31], v[72:75]
	v_mfma_f32_16x16x32_bf16 v[126:129], v[24:27], v[32:35], v[68:71]
	v_mfma_f32_16x16x32_bf16 v[68:71], v[12:15], v[64:67], v[76:79]
	v_mfma_f32_16x16x32_bf16 v[112:115], v[16:19], v[230:233], v[68:71]
	v_mfma_f32_16x16x32_bf16 v[68:71], v[20:23], v[64:67], v[80:83]
	v_mfma_f32_16x16x32_bf16 v[108:111], v[24:27], v[230:233], v[68:71]
	v_mfma_f32_16x16x32_bf16 v[68:71], v[12:15], v[234:237], v[84:87]
	v_mfma_f32_16x16x32_bf16 v[96:99], v[16:19], v[238:241], v[68:71]
	v_mfma_f32_16x16x32_bf16 v[68:71], v[20:23], v[234:237], v[88:91]
	v_mfma_f32_16x16x32_bf16 v[92:95], v[24:27], v[238:241], v[68:71]
	v_mfma_f32_16x16x32_bf16 v[68:71], v[12:15], v[242:245], v[100:103]
	v_mfma_f32_16x16x32_bf16 v[80:83], v[16:19], v[246:249], v[68:71]
	v_mfma_f32_16x16x32_bf16 v[68:71], v[20:23], v[242:245], v[104:107]
	v_mfma_f32_16x16x32_bf16 v[76:79], v[24:27], v[246:249], v[68:71]
	v_mfma_f32_16x16x32_bf16 v[68:71], v[202:205], v[28:31], v[118:121]
	v_mfma_f32_16x16x32_bf16 v[28:31], v[222:225], v[28:31], v[36:39]
	v_mfma_f32_16x16x32_bf16 v[118:121], v[226:229], v[32:35], v[28:31]
	v_mfma_f32_16x16x32_bf16 v[28:31], v[202:205], v[64:67], v[40:43]
	v_mfma_f32_16x16x32_bf16 v[104:107], v[206:209], v[230:233], v[28:31]
	v_mfma_f32_16x16x32_bf16 v[28:31], v[222:225], v[64:67], v[44:47]
	v_mfma_f32_16x16x32_bf16 v[100:103], v[226:229], v[230:233], v[28:31]
	v_mfma_f32_16x16x32_bf16 v[28:31], v[202:205], v[234:237], v[48:51]
	v_mfma_f32_16x16x32_bf16 v[88:91], v[206:209], v[238:241], v[28:31]
	v_mfma_f32_16x16x32_bf16 v[28:31], v[222:225], v[234:237], v[52:55]
	v_mfma_f32_16x16x32_bf16 v[84:87], v[226:229], v[238:241], v[28:31]
	v_mfma_f32_16x16x32_bf16 v[28:31], v[202:205], v[242:245], v[56:59]
	v_mfma_f32_16x16x32_bf16 v[72:75], v[206:209], v[246:249], v[28:31]
	v_mfma_f32_16x16x32_bf16 v[28:31], v[222:225], v[242:245], v[60:63]
	v_mfma_f32_16x16x32_bf16 v[122:125], v[206:209], v[32:35], v[68:71]
	v_mfma_f32_16x16x32_bf16 v[68:71], v[226:229], v[246:249], v[28:31]
	s_barrier
; #define PG8_MMA(ai, bj, At, Bt) do { __builtin_amdgcn_s_setprio(1); _Pragma("unroll") for (int m = 0; m < 4; ++m) _Pragma("unroll") for (int n = 0; n < 2; ++n) _Pragma("unroll") for (int k = 0; k < 2; ++k) \
;         acc[ai][bj][m][n] = __builtin_amdgcn_mfma_f32_16x16x32_bf16(Bt[n][k], At[m][k], acc[ai][bj][m][n], 0, 0, 0); __builtin_amdgcn_s_setprio(0); } while (0)
; #define PG8_WAIT_V(n) asm volatile("s_waitcnt vmcnt(" #n ")" ::: "memory")
; #define PG8_TRIP_HEAD(T) const int t = (T); const bool last = (t == nt - 2); \
;             const char* a1 = cA + (size_t)(t + 1) * kstep; \
;             const char* a2 = last ? nA : cA + (size_t)(t + 2) * kstep; const char* b2 = last ? nB : cB + (size_t)(t + 2) * kstep; \
;             const char* a3 = a2 + kstep; const char* b3 = b2 + kstep; \
;             if (last && has_next) S.a_ready(nxt);
; template <class Epi, class Sched, bool ALIGN_EPI = false, bool SP2 = false>
; __device__ __forceinline__ void gemm_phase(PG8_LAS unsigned char* lds, const Gemm g, const Sched& S, const Epi& E) {
;     ...
;         if constexpr (SP2) {
;             { PG8_TRIP_HEAD(0) PG8_TRIP_SP2(asm volatile("s_waitcnt vmcnt(%0)" :: "n"(8 + Epi::NST) : "memory"), PG8_MMAZ) }
;             for (int tt = 2; tt < nt; tt += 2) { PG8_TRIP_HEAD(tt) PG8_TRIP_SP2(PG8_WAIT_V(8), PG8_MMA) }
	s_mov_b64 s[44:45], 0x180
	s_add_i32 s39, s39, s22
	s_nop 1
	v_lshl_add_u64 v[28:29], v[250:251], 0, s[44:45]
	s_mov_b32 m0, s39
	s_mov_b64 s[42:43], 0x40180
	s_add_i32 s40, s39, 0x2000
	ds_read_b128 v[36:39], v221 offset:49152
	ds_read_b128 v[40:43], v221 offset:50176
	ds_read_b128 v[230:233], v221 offset:51200
	ds_read_b128 v[234:237], v221 offset:52224
	ds_read_b128 v[238:241], v221 offset:53248
	ds_read_b128 v[242:245], v221 offset:54272
	ds_read_b128 v[246:249], v221 offset:55296
	ds_read_b128 v[214:217], v221 offset:56320
	global_load_lds_dwordx4 v[28:29], off
	v_lshl_add_u64 v[28:29], v[250:251], 0, s[42:43]
	s_mov_b32 m0, s40
	s_mov_b64 s[42:43], 0x80180
	s_add_i32 s41, s41, s22
	global_load_lds_dwordx4 v[28:29], off
	v_lshl_add_u64 v[28:29], v[250:251], 0, s[42:43]
	s_mov_b32 m0, s41
	s_mov_b64 s[42:43], 0xc0180
	global_load_lds_dwordx4 v[28:29], off
	v_lshl_add_u64 v[28:29], v[250:251], 0, s[42:43]
	s_add_i32 s42, s41, 0x2000
	s_mov_b32 m0, s42
	s_nop 0
	global_load_lds_dwordx4 v[28:29], off
	v_lshl_add_u64 v[28:29], v[192:193], 0, s[44:45]
	s_mov_b32 m0, s27
	s_mov_b64 s[44:45], 0x42180
	global_load_lds_dwordx4 v[28:29], off
	v_lshl_add_u64 v[28:29], v[192:193], 0, s[44:45]
	s_mov_b32 m0, s28
	s_nop 0
	global_load_lds_dwordx4 v[28:29], off
	s_waitcnt vmcnt(8)
	s_waitcnt lgkmcnt(0)
	s_barrier
	v_mfma_f32_16x16x32_bf16 v[28:31], v[12:15], v[36:39], v[136:139]
	v_mfma_f32_16x16x32_bf16 v[64:67], v[16:19], v[40:43], v[28:31]
	v_mfma_f32_16x16x32_bf16 v[28:31], v[20:23], v[36:39], v[140:143]
	v_mfma_f32_16x16x32_bf16 v[60:63], v[24:27], v[40:43], v[28:31]
	v_mfma_f32_16x16x32_bf16 v[28:31], v[12:15], v[230:233], v[144:147]
	v_mfma_f32_16x16x32_bf16 v[48:51], v[16:19], v[234:237], v[28:31]
	v_mfma_f32_16x16x32_bf16 v[28:31], v[20:23], v[230:233], v[148:151]
	v_mfma_f32_16x16x32_bf16 v[44:47], v[24:27], v[234:237], v[28:31]
	v_mfma_f32_16x16x32_bf16 v[28:31], v[12:15], v[238:241], v[152:155]
	v_mfma_f32_16x16x32_bf16 v[4:7], v[12:15], v[246:249], v[4:7]
	v_mfma_f32_16x16x32_bf16 v[32:35], v[16:19], v[242:245], v[28:31]
	v_mfma_f32_16x16x32_bf16 v[28:31], v[20:23], v[238:241], v[156:159]
	v_mfma_f32_16x16x32_bf16 v[16:19], v[16:19], v[214:217], v[4:7]
	v_mfma_f32_16x16x32_bf16 v[4:7], v[20:23], v[246:249], v[8:11]
	v_mfma_f32_16x16x32_bf16 v[28:31], v[24:27], v[242:245], v[28:31]
	v_mfma_f32_16x16x32_bf16 v[12:15], v[24:27], v[214:217], v[4:7]
	v_mfma_f32_16x16x32_bf16 v[4:7], v[202:205], v[36:39], v[160:163]
	v_mfma_f32_16x16x32_bf16 v[56:59], v[206:209], v[40:43], v[4:7]
	v_mfma_f32_16x16x32_bf16 v[4:7], v[222:225], v[36:39], v[164:167]
	v_mfma_f32_16x16x32_bf16 v[52:55], v[226:229], v[40:43], v[4:7]
	v_mfma_f32_16x16x32_bf16 v[4:7], v[202:205], v[230:233], v[168:171]
	v_mfma_f32_16x16x32_bf16 v[40:43], v[206:209], v[234:237], v[4:7]
	v_mfma_f32_16x16x32_bf16 v[4:7], v[222:225], v[230:233], v[172:175]
	v_mfma_f32_16x16x32_bf16 v[36:39], v[226:229], v[234:237], v[4:7]
	v_mfma_f32_16x16x32_bf16 v[4:7], v[202:205], v[238:241], v[176:179]
	v_mfma_f32_16x16x32_bf16 v[24:27], v[206:209], v[242:245], v[4:7]
	v_mfma_f32_16x16x32_bf16 v[4:7], v[222:225], v[238:241], v[180:183]
	v_mfma_f32_16x16x32_bf16 v[20:23], v[226:229], v[242:245], v[4:7]
	v_mfma_f32_16x16x32_bf16 v[4:7], v[202:205], v[246:249], v[184:187]
	v_mfma_f32_16x16x32_bf16 v[8:11], v[206:209], v[214:217], v[4:7]
	v_mfma_f32_16x16x32_bf16 v[4:7], v[222:225], v[246:249], v[188:191]
	v_mfma_f32_16x16x32_bf16 v[4:7], v[226:229], v[214:217], v[4:7]
	s_barrier
	s_add_u32 s20, s20, 0x84180
	s_addc_u32 s21, s21, 0
	s_add_u32 s8, s8, 0x200
	s_addc_u32 s9, s9, 0
	s_mov_b64 s[48:49], 0x80000
	s_mov_b64 s[50:51], 0x80080
	s_mov_b64 s[52:53], 0xc0000
	s_mov_b64 s[54:55], 0xc0080
	s_mov_b64 s[56:57], 0xc6000
	.p2align	6

.LBB0_699:
	s_ashr_i32 s19, s18, 31
	s_lshl_b64 s[4:5], s[18:19], 20
	v_readlane_b32 s22, v254, 33
	v_readlane_b32 s23, v254, 34
	s_add_u32 s22, s22, s4
	s_addc_u32 s23, s23, s5
	s_add_i32 s33, 0, 0x10000
	s_add_i32 s41, 0, 0x14000
	v_add_u32_e32 v116, s33, v176
	v_add_u32_e32 v117, s41, v176
	ds_read_b128 v[4:7], v116
	ds_read_b128 v[8:11], v116 offset:1024
	ds_read_b128 v[12:15], v116 offset:2048
	ds_read_b128 v[16:19], v116 offset:3072
	ds_read_b128 v[20:23], v117
	ds_read_b128 v[24:27], v117 offset:1024
	ds_read_b128 v[28:31], v117 offset:2048
	ds_read_b128 v[32:35], v117 offset:3072
	s_and_b64 s[4:5], s[10:11], exec
	s_cselect_b32 s3, s23, s25
	s_cselect_b32 s4, s22, s24
	v_lshl_add_u64 v[208:209], s[26:27], 0, v[162:163]
	s_mov_b64 s[10:11], 0x84080
	s_add_i32 s5, s29, 0xc000
	v_lshl_add_u64 v[68:69], v[208:209], 0, s[10:11]
	s_mov_b32 m0, s5
	s_mov_b64 s[10:11], 0xc6080
	s_add_i32 s19, s29, 0xe000
	ds_read_b128 v[36:39], v178
	ds_read_b128 v[40:43], v178 offset:1024
	ds_read_b128 v[44:47], v178 offset:2048
	ds_read_b128 v[48:51], v178 offset:3072
	ds_read_b128 v[52:55], v178 offset:4096
	ds_read_b128 v[56:59], v178 offset:5120
	ds_read_b128 v[60:63], v178 offset:6144
	ds_read_b128 v[64:67], v178 offset:7168
	global_load_lds_dwordx4 v[68:69], off
	v_lshl_add_u64 v[68:69], v[208:209], 0, s[10:11]
	s_mov_b32 m0, s19
	s_nop 0
	global_load_lds_dwordx4 v[68:69], off
	s_waitcnt vmcnt(16)
	s_waitcnt lgkmcnt(0)
	s_barrier
	v_mfma_f32_16x16x32_bf16 v[92:95], v[4:7], v[60:63], 0
	v_mfma_f32_16x16x32_bf16 v[68:71], v[4:7], v[36:39], 0
	v_mfma_f32_16x16x32_bf16 v[72:75], v[12:15], v[36:39], 0
	v_mfma_f32_16x16x32_bf16 v[76:79], v[4:7], v[44:47], 0
	v_mfma_f32_16x16x32_bf16 v[80:83], v[12:15], v[44:47], 0
	v_mfma_f32_16x16x32_bf16 v[84:87], v[4:7], v[52:55], 0
	v_mfma_f32_16x16x32_bf16 v[88:91], v[12:15], v[52:55], 0
	v_mfma_f32_16x16x32_bf16 v[100:103], v[8:11], v[64:67], v[92:95]
	v_mfma_f32_16x16x32_bf16 v[92:95], v[12:15], v[60:63], 0
	v_mfma_f32_16x16x32_bf16 v[68:71], v[8:11], v[40:43], v[68:71]
	v_mfma_f32_16x16x32_bf16 v[72:75], v[16:19], v[40:43], v[72:75]
	v_mfma_f32_16x16x32_bf16 v[76:79], v[8:11], v[48:51], v[76:79]
	v_mfma_f32_16x16x32_bf16 v[80:83], v[16:19], v[48:51], v[80:83]
	v_mfma_f32_16x16x32_bf16 v[84:87], v[8:11], v[56:59], v[84:87]
	v_mfma_f32_16x16x32_bf16 v[88:91], v[16:19], v[56:59], v[88:91]
	v_mfma_f32_16x16x32_bf16 v[104:107], v[16:19], v[64:67], v[92:95]
	v_mfma_f32_16x16x32_bf16 v[92:95], v[20:23], v[36:39], 0
	v_mfma_f32_16x16x32_bf16 v[36:39], v[28:31], v[36:39], 0
	v_mfma_f32_16x16x32_bf16 v[120:123], v[24:27], v[40:43], v[92:95]
	v_mfma_f32_16x16x32_bf16 v[36:39], v[32:35], v[40:43], v[36:39]
	v_mfma_f32_16x16x32_bf16 v[40:43], v[20:23], v[44:47], 0
	v_mfma_f32_16x16x32_bf16 v[44:47], v[28:31], v[44:47], 0
	v_mfma_f32_16x16x32_bf16 v[40:43], v[24:27], v[48:51], v[40:43]
	v_mfma_f32_16x16x32_bf16 v[44:47], v[32:35], v[48:51], v[44:47]
	v_mfma_f32_16x16x32_bf16 v[48:51], v[20:23], v[52:55], 0
	v_mfma_f32_16x16x32_bf16 v[52:55], v[28:31], v[52:55], 0
	v_mfma_f32_16x16x32_bf16 v[48:51], v[24:27], v[56:59], v[48:51]
	v_mfma_f32_16x16x32_bf16 v[52:55], v[32:35], v[56:59], v[52:55]
	v_mfma_f32_16x16x32_bf16 v[56:59], v[20:23], v[60:63], 0
	v_mfma_f32_16x16x32_bf16 v[60:63], v[28:31], v[60:63], 0
	v_mfma_f32_16x16x32_bf16 v[56:59], v[24:27], v[64:67], v[56:59]
	v_mfma_f32_16x16x32_bf16 v[60:63], v[32:35], v[64:67], v[60:63]
	s_barrier
	v_lshl_add_u64 v[250:251], s[24:25], 0, v[160:161]
	s_mov_b64 s[10:11], 0x100
	s_add_i32 s33, s33, s28
	v_lshl_add_u64 v[118:119], v[250:251], 0, s[10:11]
	s_mov_b32 m0, s33
	s_mov_b64 s[42:43], 0x40100
	s_add_i32 s40, s33, 0x2000
	ds_read_b128 v[64:67], v178 offset:16384
	ds_read_b128 v[92:95], v178 offset:17408
	ds_read_b128 v[96:99], v178 offset:18432
	ds_read_b128 v[108:111], v178 offset:19456
	ds_read_b128 v[112:115], v178 offset:20480
	ds_read_b128 v[124:127], v178 offset:21504
	ds_read_b128 v[128:131], v178 offset:22528
	ds_read_b128 v[132:135], v178 offset:23552
	global_load_lds_dwordx4 v[118:119], off
	v_lshl_add_u64 v[118:119], v[250:251], 0, s[42:43]
	s_mov_b32 m0, s40
	s_mov_b64 s[42:43], 0x80100
	s_add_i32 s41, s41, s28
	global_load_lds_dwordx4 v[118:119], off
	v_lshl_add_u64 v[118:119], v[250:251], 0, s[42:43]
	s_mov_b32 m0, s41
	s_mov_b64 s[42:43], 0xc0100
	global_load_lds_dwordx4 v[118:119], off
	v_lshl_add_u64 v[118:119], v[250:251], 0, s[42:43]
	s_add_i32 s42, s41, 0x2000
	s_mov_b32 m0, s42
	s_nop 0
	global_load_lds_dwordx4 v[118:119], off
	v_lshl_add_u64 v[118:119], v[208:209], 0, s[10:11]
	s_mov_b32 m0, s29
	s_mov_b64 s[10:11], 0x42100
	global_load_lds_dwordx4 v[118:119], off
	v_lshl_add_u64 v[118:119], v[208:209], 0, s[10:11]
	s_mov_b32 m0, s30
	s_nop 0
	global_load_lds_dwordx4 v[118:119], off
	s_waitcnt vmcnt(16)
	s_waitcnt lgkmcnt(0)
	s_barrier
	v_mfma_f32_16x16x32_bf16 v[136:139], v[4:7], v[64:67], 0
	v_mfma_f32_16x16x32_bf16 v[144:147], v[8:11], v[92:95], v[136:139]
	v_mfma_f32_16x16x32_bf16 v[136:139], v[12:15], v[64:67], 0
	v_mfma_f32_16x16x32_bf16 v[148:151], v[16:19], v[92:95], v[136:139]
	v_mfma_f32_16x16x32_bf16 v[136:139], v[4:7], v[96:99], 0
	v_mfma_f32_16x16x32_bf16 v[152:155], v[8:11], v[108:111], v[136:139]
	v_mfma_f32_16x16x32_bf16 v[136:139], v[12:15], v[96:99], 0
	v_mfma_f32_16x16x32_bf16 v[156:159], v[16:19], v[108:111], v[136:139]
	v_mfma_f32_16x16x32_bf16 v[136:139], v[4:7], v[112:115], 0
	v_mfma_f32_16x16x32_bf16 v[4:7], v[4:7], v[128:131], 0
	v_mfma_f32_16x16x32_bf16 v[166:169], v[8:11], v[124:127], v[136:139]
	v_mfma_f32_16x16x32_bf16 v[4:7], v[8:11], v[132:135], v[4:7]
	v_mfma_f32_16x16x32_bf16 v[8:11], v[12:15], v[128:131], 0
	v_mfma_f32_16x16x32_bf16 v[136:139], v[12:15], v[112:115], 0
	v_mfma_f32_16x16x32_bf16 v[8:11], v[16:19], v[132:135], v[8:11]
	v_mfma_f32_16x16x32_bf16 v[170:173], v[16:19], v[124:127], v[136:139]
	v_mfma_f32_16x16x32_bf16 v[12:15], v[20:23], v[64:67], 0
	v_mfma_f32_16x16x32_bf16 v[180:183], v[24:27], v[92:95], v[12:15]
	v_mfma_f32_16x16x32_bf16 v[12:15], v[28:31], v[64:67], 0
	v_mfma_f32_16x16x32_bf16 v[184:187], v[32:35], v[92:95], v[12:15]
	v_mfma_f32_16x16x32_bf16 v[12:15], v[20:23], v[96:99], 0
	v_mfma_f32_16x16x32_bf16 v[188:191], v[24:27], v[108:111], v[12:15]
	v_mfma_f32_16x16x32_bf16 v[12:15], v[28:31], v[96:99], 0
	v_mfma_f32_16x16x32_bf16 v[192:195], v[32:35], v[108:111], v[12:15]
	v_mfma_f32_16x16x32_bf16 v[12:15], v[20:23], v[112:115], 0
	v_mfma_f32_16x16x32_bf16 v[196:199], v[24:27], v[124:127], v[12:15]
	v_mfma_f32_16x16x32_bf16 v[12:15], v[28:31], v[112:115], 0
	v_mfma_f32_16x16x32_bf16 v[200:203], v[32:35], v[124:127], v[12:15]
	v_mfma_f32_16x16x32_bf16 v[12:15], v[20:23], v[128:131], 0
	v_mfma_f32_16x16x32_bf16 v[204:207], v[24:27], v[132:135], v[12:15]
	v_mfma_f32_16x16x32_bf16 v[12:15], v[28:31], v[128:131], 0
	v_mfma_f32_16x16x32_bf16 v[132:135], v[32:35], v[132:135], v[12:15]
	s_barrier
	s_add_i32 s43, 0, 0x18000
	s_add_i32 s45, 0, 0x1c000
	v_add_u32_e32 v118, s43, v176
	v_add_u32_e32 v119, s45, v176
	s_nop 0
	ds_read_b128 v[12:15], v118
	ds_read_b128 v[16:19], v118 offset:1024
	ds_read_b128 v[20:23], v118 offset:2048
	ds_read_b128 v[24:27], v118 offset:3072
	ds_read_b128 v[214:217], v119
	ds_read_b128 v[218:221], v119 offset:1024
	ds_read_b128 v[222:225], v119 offset:2048
	ds_read_b128 v[226:229], v119 offset:3072
	s_mov_b64 s[10:11], 0x84100
	s_mov_b32 m0, s31
	v_lshl_add_u64 v[92:93], v[208:209], 0, s[10:11]
	s_mov_b64 s[10:11], 0xc6100
	ds_read_b128 v[28:31], v178 offset:32768
	ds_read_b128 v[32:35], v178 offset:33792
	ds_read_b128 v[64:67], v178 offset:34816
	ds_read_b128 v[230:233], v178 offset:35840
	ds_read_b128 v[234:237], v178 offset:36864
	ds_read_b128 v[238:241], v178 offset:37888
	ds_read_b128 v[242:245], v178 offset:38912
	ds_read_b128 v[246:249], v178 offset:39936
	global_load_lds_dwordx4 v[92:93], off
	v_lshl_add_u64 v[92:93], v[208:209], 0, s[10:11]
	s_mov_b32 m0, s34
	s_nop 0
	global_load_lds_dwordx4 v[92:93], off
	s_waitcnt vmcnt(8)
	s_waitcnt lgkmcnt(0)
	s_barrier
	v_mfma_f32_16x16x32_bf16 v[68:71], v[12:15], v[28:31], v[68:71]
	v_mfma_f32_16x16x32_bf16 v[140:143], v[16:19], v[32:35], v[68:71]
	v_mfma_f32_16x16x32_bf16 v[68:71], v[20:23], v[28:31], v[72:75]
	v_mfma_f32_16x16x32_bf16 v[136:139], v[24:27], v[32:35], v[68:71]
	v_mfma_f32_16x16x32_bf16 v[68:71], v[12:15], v[64:67], v[76:79]
	v_mfma_f32_16x16x32_bf16 v[112:115], v[16:19], v[230:233], v[68:71]
	v_mfma_f32_16x16x32_bf16 v[68:71], v[20:23], v[64:67], v[80:83]
	v_mfma_f32_16x16x32_bf16 v[108:111], v[24:27], v[230:233], v[68:71]
	v_mfma_f32_16x16x32_bf16 v[68:71], v[12:15], v[234:237], v[84:87]
	v_mfma_f32_16x16x32_bf16 v[96:99], v[16:19], v[238:241], v[68:71]
	v_mfma_f32_16x16x32_bf16 v[68:71], v[20:23], v[234:237], v[88:91]
	v_mfma_f32_16x16x32_bf16 v[92:95], v[24:27], v[238:241], v[68:71]
	v_mfma_f32_16x16x32_bf16 v[68:71], v[12:15], v[242:245], v[100:103]
	v_mfma_f32_16x16x32_bf16 v[80:83], v[16:19], v[246:249], v[68:71]
	v_mfma_f32_16x16x32_bf16 v[68:71], v[20:23], v[242:245], v[104:107]
	v_mfma_f32_16x16x32_bf16 v[76:79], v[24:27], v[246:249], v[68:71]
	v_mfma_f32_16x16x32_bf16 v[68:71], v[214:217], v[28:31], v[120:123]
	v_mfma_f32_16x16x32_bf16 v[28:31], v[222:225], v[28:31], v[36:39]
	v_mfma_f32_16x16x32_bf16 v[124:127], v[226:229], v[32:35], v[28:31]
	v_mfma_f32_16x16x32_bf16 v[28:31], v[214:217], v[64:67], v[40:43]
	v_mfma_f32_16x16x32_bf16 v[104:107], v[218:221], v[230:233], v[28:31]
	v_mfma_f32_16x16x32_bf16 v[28:31], v[222:225], v[64:67], v[44:47]
	v_mfma_f32_16x16x32_bf16 v[100:103], v[226:229], v[230:233], v[28:31]
	v_mfma_f32_16x16x32_bf16 v[28:31], v[214:217], v[234:237], v[48:51]
	v_mfma_f32_16x16x32_bf16 v[88:91], v[218:221], v[238:241], v[28:31]
	v_mfma_f32_16x16x32_bf16 v[28:31], v[222:225], v[234:237], v[52:55]
	v_mfma_f32_16x16x32_bf16 v[84:87], v[226:229], v[238:241], v[28:31]
	v_mfma_f32_16x16x32_bf16 v[28:31], v[214:217], v[242:245], v[56:59]
	v_mfma_f32_16x16x32_bf16 v[72:75], v[218:221], v[246:249], v[28:31]
	v_mfma_f32_16x16x32_bf16 v[28:31], v[222:225], v[242:245], v[60:63]
	v_mfma_f32_16x16x32_bf16 v[128:131], v[218:221], v[32:35], v[68:71]
	v_mfma_f32_16x16x32_bf16 v[68:71], v[226:229], v[246:249], v[28:31]
	s_barrier
; #define PG8_MMA(ai, bj, At, Bt) do { __builtin_amdgcn_s_setprio(1); _Pragma("unroll") for (int m = 0; m < 4; ++m) _Pragma("unroll") for (int n = 0; n < 2; ++n) _Pragma("unroll") for (int k = 0; k < 2; ++k) \
;         acc[ai][bj][m][n] = __builtin_amdgcn_mfma_f32_16x16x32_bf16(Bt[n][k], At[m][k], acc[ai][bj][m][n], 0, 0, 0); __builtin_amdgcn_s_setprio(0); } while (0)
; #define PG8_WAIT_V(n) asm volatile("s_waitcnt vmcnt(" #n ")" ::: "memory")
; #define PG8_TRIP_HEAD(T) const int t = (T); const bool last = (t == nt - 2); \
;             const char* a1 = cA + (size_t)(t + 1) * kstep; \
;             const char* a2 = last ? nA : cA + (size_t)(t + 2) * kstep; const char* b2 = last ? nB : cB + (size_t)(t + 2) * kstep; \
;             const char* a3 = a2 + kstep; const char* b3 = b2 + kstep; \
;             if (last && has_next) S.a_ready(nxt);
; template <class Epi, class Sched, bool ALIGN_EPI = false, bool SP2 = false>
; __device__ __forceinline__ void gemm_phase(PG8_LAS unsigned char* lds, const Gemm g, const Sched& S, const Epi& E) {
;     ...
;         if constexpr (SP2) {
;             { PG8_TRIP_HEAD(0) PG8_TRIP_SP2(asm volatile("s_waitcnt vmcnt(%0)" :: "n"(8 + Epi::NST) : "memory"), PG8_MMAZ) }
;             for (int tt = 2; tt < nt; tt += 2) { PG8_TRIP_HEAD(tt) PG8_TRIP_SP2(PG8_WAIT_V(8), PG8_MMA) }
	s_mov_b64 s[10:11], 0x180
	s_add_i32 s43, s43, s28
	s_nop 1
	v_lshl_add_u64 v[28:29], v[250:251], 0, s[10:11]
	s_mov_b32 m0, s43
	s_mov_b64 s[46:47], 0x40180
	s_add_i32 s44, s43, 0x2000
	ds_read_b128 v[36:39], v178 offset:49152
	ds_read_b128 v[40:43], v178 offset:50176
	ds_read_b128 v[120:123], v178 offset:51200
	ds_read_b128 v[230:233], v178 offset:52224
	ds_read_b128 v[234:237], v178 offset:53248
	ds_read_b128 v[238:241], v178 offset:54272
	ds_read_b128 v[242:245], v178 offset:55296
	ds_read_b128 v[246:249], v178 offset:56320
	global_load_lds_dwordx4 v[28:29], off
	v_lshl_add_u64 v[28:29], v[250:251], 0, s[46:47]
	s_mov_b32 m0, s44
	s_mov_b64 s[46:47], 0x80180
	s_add_i32 s45, s45, s28
	global_load_lds_dwordx4 v[28:29], off
	v_lshl_add_u64 v[28:29], v[250:251], 0, s[46:47]
	s_mov_b32 m0, s45
	s_mov_b64 s[46:47], 0xc0180
	global_load_lds_dwordx4 v[28:29], off
	v_lshl_add_u64 v[28:29], v[250:251], 0, s[46:47]
	s_add_i32 s46, s45, 0x2000
	s_mov_b32 m0, s46
	s_nop 0
	global_load_lds_dwordx4 v[28:29], off
	v_lshl_add_u64 v[28:29], v[208:209], 0, s[10:11]
	s_mov_b32 m0, s36
	s_mov_b64 s[10:11], 0x42180
	global_load_lds_dwordx4 v[28:29], off
	v_lshl_add_u64 v[28:29], v[208:209], 0, s[10:11]
	s_mov_b32 m0, s37
	s_nop 0
	global_load_lds_dwordx4 v[28:29], off
	s_waitcnt vmcnt(8)
	s_waitcnt lgkmcnt(0)
	s_barrier
	v_mfma_f32_16x16x32_bf16 v[28:31], v[12:15], v[36:39], v[144:147]
	v_mfma_f32_16x16x32_bf16 v[56:59], v[16:19], v[40:43], v[28:31]
	v_mfma_f32_16x16x32_bf16 v[28:31], v[20:23], v[36:39], v[148:151]
	v_mfma_f32_16x16x32_bf16 v[52:55], v[24:27], v[40:43], v[28:31]
	v_mfma_f32_16x16x32_bf16 v[28:31], v[12:15], v[120:123], v[152:155]
	v_mfma_f32_16x16x32_bf16 v[48:51], v[16:19], v[230:233], v[28:31]
	v_mfma_f32_16x16x32_bf16 v[28:31], v[20:23], v[120:123], v[156:159]
	v_mfma_f32_16x16x32_bf16 v[44:47], v[24:27], v[230:233], v[28:31]
	v_mfma_f32_16x16x32_bf16 v[28:31], v[12:15], v[234:237], v[166:169]
	v_mfma_f32_16x16x32_bf16 v[4:7], v[12:15], v[242:245], v[4:7]
	v_mfma_f32_16x16x32_bf16 v[32:35], v[16:19], v[238:241], v[28:31]
	v_mfma_f32_16x16x32_bf16 v[28:31], v[20:23], v[234:237], v[170:173]
	v_mfma_f32_16x16x32_bf16 v[16:19], v[16:19], v[246:249], v[4:7]
	v_mfma_f32_16x16x32_bf16 v[4:7], v[20:23], v[242:245], v[8:11]
	v_mfma_f32_16x16x32_bf16 v[28:31], v[24:27], v[238:241], v[28:31]
	v_mfma_f32_16x16x32_bf16 v[12:15], v[24:27], v[246:249], v[4:7]
	v_mfma_f32_16x16x32_bf16 v[4:7], v[214:217], v[36:39], v[180:183]
	v_mfma_f32_16x16x32_bf16 v[64:67], v[218:221], v[40:43], v[4:7]
	v_mfma_f32_16x16x32_bf16 v[4:7], v[222:225], v[36:39], v[184:187]
	v_mfma_f32_16x16x32_bf16 v[60:63], v[226:229], v[40:43], v[4:7]
	v_mfma_f32_16x16x32_bf16 v[4:7], v[214:217], v[120:123], v[188:191]
	v_mfma_f32_16x16x32_bf16 v[40:43], v[218:221], v[230:233], v[4:7]
	v_mfma_f32_16x16x32_bf16 v[4:7], v[222:225], v[120:123], v[192:195]
	v_mfma_f32_16x16x32_bf16 v[36:39], v[226:229], v[230:233], v[4:7]
	v_mfma_f32_16x16x32_bf16 v[4:7], v[214:217], v[234:237], v[196:199]
	v_mfma_f32_16x16x32_bf16 v[24:27], v[218:221], v[238:241], v[4:7]
	v_mfma_f32_16x16x32_bf16 v[4:7], v[222:225], v[234:237], v[200:203]
	v_mfma_f32_16x16x32_bf16 v[20:23], v[226:229], v[238:241], v[4:7]
	v_mfma_f32_16x16x32_bf16 v[4:7], v[214:217], v[242:245], v[204:207]
	v_mfma_f32_16x16x32_bf16 v[8:11], v[218:221], v[246:249], v[4:7]
	v_mfma_f32_16x16x32_bf16 v[4:7], v[222:225], v[242:245], v[132:135]
	v_mfma_f32_16x16x32_bf16 v[4:7], v[226:229], v[246:249], v[4:7]
	s_barrier
	s_add_u32 s10, s26, 0x84180
	s_addc_u32 s11, s27, 0
	s_add_u32 s24, s24, 0x200
	s_addc_u32 s25, s25, 0
	s_mov_b32 s26, 0
	s_mov_b64 s[52:53], 0x80000
	s_mov_b64 s[54:55], 0x80080
	s_mov_b64 s[56:57], 0xc0000
	s_mov_b64 s[60:61], 0xc0080
	s_mov_b64 s[62:63], 0xc6000
	.p2align	6
